# GEMM K-loops: the leading half waits for its staged pieces at the end of its compute segment (all six loops)
# baseline (speedup 1.0000x reference)
.LBB0_1128:
	s_ashr_i32 s21, s20, 31
	s_lshl_b64 s[0:1], s[20:21], 20
	s_add_u32 s22, s36, s0
	s_addc_u32 s23, s37, s1
	s_and_b64 s[0:1], s[4:5], exec
	s_cselect_b32 s21, s23, s31
	s_cselect_b32 s52, s22, s30
	s_ashr_i32 s19, s18, 31
	s_lshl_b64 s[0:1], s[18:19], 20
	s_add_u32 s24, s38, s0
	s_addc_u32 s25, s39, s1
	s_and_b64 s[0:1], s[4:5], exec
	s_cselect_b32 s19, s25, s29
	s_cselect_b32 s53, s24, s28
	s_add_u32 s54, s28, 0x4000
	s_addc_u32 s55, s29, 0
	s_add_u32 s28, s30, 0x80080
	s_addc_u32 s29, s31, 0
	s_mov_b32 s56, -2
	ds_read_b128 v[146:149], v164
	ds_read_b128 v[150:153], v164 offset:1024
	ds_read_b128 v[168:171], v164 offset:2048
	ds_read_b128 v[172:175], v164 offset:3072
	ds_read_b128 v[176:179], v165
	ds_read_b128 v[180:183], v165 offset:1024
	ds_read_b128 v[184:187], v165 offset:2048
	ds_read_b128 v[188:191], v165 offset:3072
	s_add_u32 s0, s28, 0xfff80080
	s_addc_u32 s1, s29, -1
	s_cmp_eq_u32 s56, 28
	s_cselect_b32 s35, s21, s1
	s_cselect_b32 s34, s52, s0
	s_cselect_b32 s31, s19, s55
	s_cselect_b32 s30, s53, s54
	v_lshl_add_u64 v[224:225], s[28:29], 0, v[138:139]
	s_add_i32 m0, s27, 0xc000
	ds_read_b128 v[192:195], v166
	ds_read_b128 v[196:199], v166 offset:1024
	ds_read_b128 v[200:203], v166 offset:2048
	ds_read_b128 v[204:207], v166 offset:3072
	ds_read_b128 v[208:211], v166 offset:4096
	ds_read_b128 v[212:215], v166 offset:5120
	ds_read_b128 v[216:219], v166 offset:6144
	ds_read_b128 v[220:223], v166 offset:7168
	global_load_lds_dwordx4 v[224:225], off
	v_lshl_add_u64 v[224:225], s[28:29], 0, v[140:141]
	s_add_i32 m0, s27, 0xe000
	s_nop 0
	global_load_lds_dwordx4 v[224:225], off
	s_and_b64 vcc, exec, s[14:15]
	s_cbranch_vccnz .Lwa_1129p_0
	s_waitcnt vmcnt(8)
.Lwa_1129p_0:
	s_waitcnt lgkmcnt(0)
	s_barrier
	s_setprio 1
	s_waitcnt lgkmcnt(0)
	v_mfma_f32_16x16x32_bf16 v[126:129], v[146:149], v[192:195], 0
	v_mfma_f32_16x16x32_bf16 v[122:125], v[168:171], v[192:195], 0
	v_mfma_f32_16x16x32_bf16 v[110:113], v[146:149], v[200:203], 0
	v_mfma_f32_16x16x32_bf16 v[106:109], v[168:171], v[200:203], 0
	v_mfma_f32_16x16x32_bf16 v[94:97], v[146:149], v[208:211], 0
	v_mfma_f32_16x16x32_bf16 v[90:93], v[168:171], v[208:211], 0
	v_mfma_f32_16x16x32_bf16 v[78:81], v[146:149], v[216:219], 0
	v_mfma_f32_16x16x32_bf16 v[74:77], v[168:171], v[216:219], 0
	v_mfma_f32_16x16x32_bf16 v[126:129], v[150:153], v[196:199], v[126:129]
	v_mfma_f32_16x16x32_bf16 v[122:125], v[172:175], v[196:199], v[122:125]
	v_mfma_f32_16x16x32_bf16 v[110:113], v[150:153], v[204:207], v[110:113]
	v_mfma_f32_16x16x32_bf16 v[106:109], v[172:175], v[204:207], v[106:109]
	v_mfma_f32_16x16x32_bf16 v[94:97], v[150:153], v[212:215], v[94:97]
	v_mfma_f32_16x16x32_bf16 v[90:93], v[172:175], v[212:215], v[90:93]
	v_mfma_f32_16x16x32_bf16 v[78:81], v[150:153], v[220:223], v[78:81]
	v_mfma_f32_16x16x32_bf16 v[74:77], v[172:175], v[220:223], v[74:77]
	s_setprio 0
	s_setprio 1
	v_mfma_f32_16x16x32_bf16 v[118:121], v[176:179], v[192:195], 0
	v_mfma_f32_16x16x32_bf16 v[114:117], v[184:187], v[192:195], 0
	v_mfma_f32_16x16x32_bf16 v[102:105], v[176:179], v[200:203], 0
	v_mfma_f32_16x16x32_bf16 v[98:101], v[184:187], v[200:203], 0
	v_mfma_f32_16x16x32_bf16 v[86:89], v[176:179], v[208:211], 0
	v_mfma_f32_16x16x32_bf16 v[82:85], v[184:187], v[208:211], 0
	v_mfma_f32_16x16x32_bf16 v[70:73], v[176:179], v[216:219], 0
	v_mfma_f32_16x16x32_bf16 v[66:69], v[184:187], v[216:219], 0
	v_mfma_f32_16x16x32_bf16 v[118:121], v[180:183], v[196:199], v[118:121]
	v_mfma_f32_16x16x32_bf16 v[114:117], v[188:191], v[196:199], v[114:117]
	v_mfma_f32_16x16x32_bf16 v[102:105], v[180:183], v[204:207], v[102:105]
	v_mfma_f32_16x16x32_bf16 v[98:101], v[188:191], v[204:207], v[98:101]
	v_mfma_f32_16x16x32_bf16 v[86:89], v[180:183], v[212:215], v[86:89]
	v_mfma_f32_16x16x32_bf16 v[82:85], v[188:191], v[212:215], v[82:85]
	v_mfma_f32_16x16x32_bf16 v[70:73], v[180:183], v[220:223], v[70:73]
	v_mfma_f32_16x16x32_bf16 v[66:69], v[188:191], v[220:223], v[66:69]
	s_cbranch_vccz .Lwb_1129p_0
	s_waitcnt vmcnt(8)
.Lwb_1129p_0:
	s_setprio 0
	s_barrier
	s_add_i32 s0, s48, s40
	v_lshl_add_u64 v[224:225], s[30:31], 0, v[132:133]
	s_mov_b32 m0, s0
	ds_read_b128 v[192:195], v166 offset:16384
	ds_read_b128 v[196:199], v166 offset:17408
	ds_read_b128 v[200:203], v166 offset:18432
	ds_read_b128 v[204:207], v166 offset:19456
	ds_read_b128 v[208:211], v166 offset:20480
	ds_read_b128 v[212:215], v166 offset:21504
	ds_read_b128 v[216:219], v166 offset:22528
	ds_read_b128 v[220:223], v166 offset:23552
	global_load_lds_dwordx4 v[224:225], off
	s_add_i32 m0, s0, 0x2000
	s_add_u32 s0, s30, 0x80000
	v_lshl_add_u64 v[224:225], s[30:31], 0, v[136:137]
	s_addc_u32 s1, s31, 0
	s_add_i32 s2, s49, s40
	global_load_lds_dwordx4 v[224:225], off
	v_lshl_add_u64 v[224:225], s[0:1], 0, v[132:133]
	s_mov_b32 m0, s2
	v_lshl_add_u64 v[226:227], s[34:35], 0, v[134:135]
	global_load_lds_dwordx4 v[224:225], off
	v_lshl_add_u64 v[224:225], s[0:1], 0, v[136:137]
	s_add_i32 m0, s2, 0x2000
	s_nop 0
	global_load_lds_dwordx4 v[224:225], off
	v_lshl_add_u64 v[224:225], s[34:35], 0, v[130:131]
	s_mov_b32 m0, s27
	s_nop 0
	global_load_lds_dwordx4 v[224:225], off
	s_mov_b32 m0, s41
	s_nop 0
	global_load_lds_dwordx4 v[226:227], off
	s_and_b64 vcc, exec, s[14:15]
	s_cbranch_vccnz .Lwa_1129p_1
	s_waitcnt vmcnt(8)
.Lwa_1129p_1:
	s_waitcnt lgkmcnt(0)
	s_barrier
	s_setprio 1
	s_waitcnt lgkmcnt(0)
	v_mfma_f32_16x16x32_bf16 v[62:65], v[146:149], v[192:195], 0
	v_mfma_f32_16x16x32_bf16 v[58:61], v[168:171], v[192:195], 0
	v_mfma_f32_16x16x32_bf16 v[46:49], v[146:149], v[200:203], 0
	v_mfma_f32_16x16x32_bf16 v[42:45], v[168:171], v[200:203], 0
	v_mfma_f32_16x16x32_bf16 v[30:33], v[146:149], v[208:211], 0
	v_mfma_f32_16x16x32_bf16 v[26:29], v[168:171], v[208:211], 0
	v_mfma_f32_16x16x32_bf16 v[14:17], v[146:149], v[216:219], 0
	v_mfma_f32_16x16x32_bf16 v[10:13], v[168:171], v[216:219], 0
	v_mfma_f32_16x16x32_bf16 v[62:65], v[150:153], v[196:199], v[62:65]
	v_mfma_f32_16x16x32_bf16 v[58:61], v[172:175], v[196:199], v[58:61]
	v_mfma_f32_16x16x32_bf16 v[46:49], v[150:153], v[204:207], v[46:49]
	v_mfma_f32_16x16x32_bf16 v[42:45], v[172:175], v[204:207], v[42:45]
	v_mfma_f32_16x16x32_bf16 v[30:33], v[150:153], v[212:215], v[30:33]
	v_mfma_f32_16x16x32_bf16 v[26:29], v[172:175], v[212:215], v[26:29]
	v_mfma_f32_16x16x32_bf16 v[14:17], v[150:153], v[220:223], v[14:17]
	v_mfma_f32_16x16x32_bf16 v[10:13], v[172:175], v[220:223], v[10:13]
	s_setprio 0
	s_setprio 1
	v_mfma_f32_16x16x32_bf16 v[54:57], v[176:179], v[192:195], 0
	v_mfma_f32_16x16x32_bf16 v[50:53], v[184:187], v[192:195], 0
	v_mfma_f32_16x16x32_bf16 v[38:41], v[176:179], v[200:203], 0
	v_mfma_f32_16x16x32_bf16 v[34:37], v[184:187], v[200:203], 0
	v_mfma_f32_16x16x32_bf16 v[22:25], v[176:179], v[208:211], 0
	v_mfma_f32_16x16x32_bf16 v[18:21], v[184:187], v[208:211], 0
	v_mfma_f32_16x16x32_bf16 v[6:9], v[176:179], v[216:219], 0
	v_mfma_f32_16x16x32_bf16 v[2:5], v[184:187], v[216:219], 0
	v_mfma_f32_16x16x32_bf16 v[54:57], v[180:183], v[196:199], v[54:57]
	v_mfma_f32_16x16x32_bf16 v[50:53], v[188:191], v[196:199], v[50:53]
	v_mfma_f32_16x16x32_bf16 v[38:41], v[180:183], v[204:207], v[38:41]
	v_mfma_f32_16x16x32_bf16 v[34:37], v[188:191], v[204:207], v[34:37]
	v_mfma_f32_16x16x32_bf16 v[22:25], v[180:183], v[212:215], v[22:25]
	v_mfma_f32_16x16x32_bf16 v[18:21], v[188:191], v[212:215], v[18:21]
	v_mfma_f32_16x16x32_bf16 v[6:9], v[180:183], v[220:223], v[6:9]
	v_mfma_f32_16x16x32_bf16 v[2:5], v[188:191], v[220:223], v[2:5]
	s_cbranch_vccz .Lwb_1129p_1
	s_waitcnt vmcnt(8)

.LBB0_1129:
	ds_read_b128 v[146:149], v164
	ds_read_b128 v[150:153], v164 offset:1024
	ds_read_b128 v[168:171], v164 offset:2048
	ds_read_b128 v[172:175], v164 offset:3072
	ds_read_b128 v[176:179], v165
	ds_read_b128 v[180:183], v165 offset:1024
	ds_read_b128 v[184:187], v165 offset:2048
	ds_read_b128 v[188:191], v165 offset:3072
	s_add_u32 s0, s28, 0xfff80080
	s_addc_u32 s1, s29, -1
	s_cmp_eq_u32 s56, 28
	s_cselect_b32 s35, s21, s1
	s_cselect_b32 s34, s52, s0
	s_cselect_b32 s31, s19, s55
	s_cselect_b32 s30, s53, s54
	v_lshl_add_u64 v[224:225], s[28:29], 0, v[138:139]
	s_add_i32 m0, s27, 0xc000
	ds_read_b128 v[192:195], v166
	ds_read_b128 v[196:199], v166 offset:1024
	ds_read_b128 v[200:203], v166 offset:2048
	ds_read_b128 v[204:207], v166 offset:3072
	ds_read_b128 v[208:211], v166 offset:4096
	ds_read_b128 v[212:215], v166 offset:5120
	ds_read_b128 v[216:219], v166 offset:6144
	ds_read_b128 v[220:223], v166 offset:7168
	global_load_lds_dwordx4 v[224:225], off
	v_lshl_add_u64 v[224:225], s[28:29], 0, v[140:141]
	s_add_i32 m0, s27, 0xe000
	s_nop 0
	global_load_lds_dwordx4 v[224:225], off
	s_and_b64 vcc, exec, s[14:15]
	s_cbranch_vccnz .Lwa_1129l_0
	s_waitcnt vmcnt(8)
.Lwa_1129l_0:
	s_waitcnt lgkmcnt(0)
	s_barrier
	s_setprio 1
	s_waitcnt lgkmcnt(0)
	v_mfma_f32_16x16x32_bf16 v[126:129], v[146:149], v[192:195], v[126:129]
	v_mfma_f32_16x16x32_bf16 v[122:125], v[168:171], v[192:195], v[122:125]
	v_mfma_f32_16x16x32_bf16 v[110:113], v[146:149], v[200:203], v[110:113]
	v_mfma_f32_16x16x32_bf16 v[106:109], v[168:171], v[200:203], v[106:109]
	v_mfma_f32_16x16x32_bf16 v[94:97], v[146:149], v[208:211], v[94:97]
	v_mfma_f32_16x16x32_bf16 v[90:93], v[168:171], v[208:211], v[90:93]
	v_mfma_f32_16x16x32_bf16 v[78:81], v[146:149], v[216:219], v[78:81]
	v_mfma_f32_16x16x32_bf16 v[74:77], v[168:171], v[216:219], v[74:77]
	v_mfma_f32_16x16x32_bf16 v[126:129], v[150:153], v[196:199], v[126:129]
	v_mfma_f32_16x16x32_bf16 v[122:125], v[172:175], v[196:199], v[122:125]
	v_mfma_f32_16x16x32_bf16 v[110:113], v[150:153], v[204:207], v[110:113]
	v_mfma_f32_16x16x32_bf16 v[106:109], v[172:175], v[204:207], v[106:109]
	v_mfma_f32_16x16x32_bf16 v[94:97], v[150:153], v[212:215], v[94:97]
	v_mfma_f32_16x16x32_bf16 v[90:93], v[172:175], v[212:215], v[90:93]
	v_mfma_f32_16x16x32_bf16 v[78:81], v[150:153], v[220:223], v[78:81]
	v_mfma_f32_16x16x32_bf16 v[74:77], v[172:175], v[220:223], v[74:77]
	s_setprio 0
	s_setprio 1
	v_mfma_f32_16x16x32_bf16 v[118:121], v[176:179], v[192:195], v[118:121]
	v_mfma_f32_16x16x32_bf16 v[114:117], v[184:187], v[192:195], v[114:117]
	v_mfma_f32_16x16x32_bf16 v[102:105], v[176:179], v[200:203], v[102:105]
	v_mfma_f32_16x16x32_bf16 v[98:101], v[184:187], v[200:203], v[98:101]
	v_mfma_f32_16x16x32_bf16 v[86:89], v[176:179], v[208:211], v[86:89]
	v_mfma_f32_16x16x32_bf16 v[82:85], v[184:187], v[208:211], v[82:85]
	v_mfma_f32_16x16x32_bf16 v[70:73], v[176:179], v[216:219], v[70:73]
	v_mfma_f32_16x16x32_bf16 v[66:69], v[184:187], v[216:219], v[66:69]
	v_mfma_f32_16x16x32_bf16 v[118:121], v[180:183], v[196:199], v[118:121]
	v_mfma_f32_16x16x32_bf16 v[114:117], v[188:191], v[196:199], v[114:117]
	v_mfma_f32_16x16x32_bf16 v[102:105], v[180:183], v[204:207], v[102:105]
	v_mfma_f32_16x16x32_bf16 v[98:101], v[188:191], v[204:207], v[98:101]
	v_mfma_f32_16x16x32_bf16 v[86:89], v[180:183], v[212:215], v[86:89]
	v_mfma_f32_16x16x32_bf16 v[82:85], v[188:191], v[212:215], v[82:85]
	v_mfma_f32_16x16x32_bf16 v[70:73], v[180:183], v[220:223], v[70:73]
	v_mfma_f32_16x16x32_bf16 v[66:69], v[188:191], v[220:223], v[66:69]
	s_cbranch_vccz .Lwb_1129l_0
	s_waitcnt vmcnt(8)

.Lwa_1129l_1:
	s_waitcnt lgkmcnt(0)
	s_barrier
	s_setprio 1
	s_waitcnt lgkmcnt(0)
	v_mfma_f32_16x16x32_bf16 v[62:65], v[146:149], v[192:195], v[62:65]
	v_mfma_f32_16x16x32_bf16 v[58:61], v[168:171], v[192:195], v[58:61]
	v_mfma_f32_16x16x32_bf16 v[46:49], v[146:149], v[200:203], v[46:49]
	v_mfma_f32_16x16x32_bf16 v[42:45], v[168:171], v[200:203], v[42:45]
	v_mfma_f32_16x16x32_bf16 v[30:33], v[146:149], v[208:211], v[30:33]
	v_mfma_f32_16x16x32_bf16 v[26:29], v[168:171], v[208:211], v[26:29]
	v_mfma_f32_16x16x32_bf16 v[14:17], v[146:149], v[216:219], v[14:17]
	v_mfma_f32_16x16x32_bf16 v[10:13], v[168:171], v[216:219], v[10:13]
	v_mfma_f32_16x16x32_bf16 v[62:65], v[150:153], v[196:199], v[62:65]
	v_mfma_f32_16x16x32_bf16 v[58:61], v[172:175], v[196:199], v[58:61]
	v_mfma_f32_16x16x32_bf16 v[46:49], v[150:153], v[204:207], v[46:49]
	v_mfma_f32_16x16x32_bf16 v[42:45], v[172:175], v[204:207], v[42:45]
	v_mfma_f32_16x16x32_bf16 v[30:33], v[150:153], v[212:215], v[30:33]
	v_mfma_f32_16x16x32_bf16 v[26:29], v[172:175], v[212:215], v[26:29]
	v_mfma_f32_16x16x32_bf16 v[14:17], v[150:153], v[220:223], v[14:17]
	v_mfma_f32_16x16x32_bf16 v[10:13], v[172:175], v[220:223], v[10:13]
	s_setprio 0
	s_setprio 1
	v_mfma_f32_16x16x32_bf16 v[54:57], v[176:179], v[192:195], v[54:57]
	v_mfma_f32_16x16x32_bf16 v[50:53], v[184:187], v[192:195], v[50:53]
	v_mfma_f32_16x16x32_bf16 v[38:41], v[176:179], v[200:203], v[38:41]
	v_mfma_f32_16x16x32_bf16 v[34:37], v[184:187], v[200:203], v[34:37]
	v_mfma_f32_16x16x32_bf16 v[22:25], v[176:179], v[208:211], v[22:25]
	v_mfma_f32_16x16x32_bf16 v[18:21], v[184:187], v[208:211], v[18:21]
	v_mfma_f32_16x16x32_bf16 v[6:9], v[176:179], v[216:219], v[6:9]
	v_mfma_f32_16x16x32_bf16 v[2:5], v[184:187], v[216:219], v[2:5]
	v_mfma_f32_16x16x32_bf16 v[54:57], v[180:183], v[196:199], v[54:57]
	v_mfma_f32_16x16x32_bf16 v[50:53], v[188:191], v[196:199], v[50:53]
	v_mfma_f32_16x16x32_bf16 v[38:41], v[180:183], v[204:207], v[38:41]
	v_mfma_f32_16x16x32_bf16 v[34:37], v[188:191], v[204:207], v[34:37]
	v_mfma_f32_16x16x32_bf16 v[22:25], v[180:183], v[212:215], v[22:25]
	v_mfma_f32_16x16x32_bf16 v[18:21], v[188:191], v[212:215], v[18:21]
	v_mfma_f32_16x16x32_bf16 v[6:9], v[180:183], v[220:223], v[6:9]
	v_mfma_f32_16x16x32_bf16 v[2:5], v[188:191], v[220:223], v[2:5]
	s_cbranch_vccz .Lwb_1129l_1
	s_waitcnt vmcnt(8)

.Lmid_1129:
	s_add_i32 s2, 0, 0x18000
	v_add_u32_e32 v0, s2, v162
	s_add_i32 s3, 0, 0x1c000
	ds_read_b128 v[146:149], v0
	ds_read_b128 v[150:153], v0 offset:1024
	ds_read_b128 v[168:171], v0 offset:2048
	ds_read_b128 v[172:175], v0 offset:3072
	v_add_u32_e32 v0, s3, v162
	ds_read_b128 v[176:179], v0
	ds_read_b128 v[180:183], v0 offset:1024
	ds_read_b128 v[184:187], v0 offset:2048
	ds_read_b128 v[188:191], v0 offset:3072
	s_add_u32 s0, s34, 0x80000
	s_addc_u32 s1, s35, 0
	s_mov_b32 m0, s42
	v_lshl_add_u64 v[228:229], s[0:1], 0, v[130:131]
	ds_read_b128 v[192:195], v166 offset:32768
	ds_read_b128 v[196:199], v166 offset:33792
	ds_read_b128 v[200:203], v166 offset:34816
	ds_read_b128 v[204:207], v166 offset:35840
	ds_read_b128 v[208:211], v166 offset:36864
	ds_read_b128 v[212:215], v166 offset:37888
	ds_read_b128 v[216:219], v166 offset:38912
	ds_read_b128 v[220:223], v166 offset:39936
	global_load_lds_dwordx4 v[228:229], off
	v_lshl_add_u64 v[228:229], s[0:1], 0, v[134:135]
	s_mov_b32 m0, s43
	s_nop 0
	global_load_lds_dwordx4 v[228:229], off
	s_and_b64 vcc, exec, s[14:15]
	s_cbranch_vccnz .Lwa_1129l_2
	s_waitcnt vmcnt(8)

.Lwb_1129l_2:
	s_setprio 0
	s_barrier
	s_add_u32 s0, s30, 0x2000
	s_addc_u32 s1, s31, 0
	s_add_i32 s2, s2, s40
	v_lshl_add_u64 v[228:229], s[0:1], 0, v[132:133]
	s_mov_b32 m0, s2
	ds_read_b128 v[192:195], v166 offset:49152
	ds_read_b128 v[196:199], v166 offset:50176
	ds_read_b128 v[200:203], v166 offset:51200
	ds_read_b128 v[204:207], v166 offset:52224
	ds_read_b128 v[208:211], v166 offset:53248
	ds_read_b128 v[212:215], v166 offset:54272
	ds_read_b128 v[216:219], v166 offset:55296
	ds_read_b128 v[220:223], v166 offset:56320
	global_load_lds_dwordx4 v[228:229], off
	s_add_i32 m0, s2, 0x2000
	v_lshl_add_u64 v[228:229], s[0:1], 0, v[136:137]
	s_add_u32 s0, s30, 0x82000
	s_addc_u32 s1, s31, 0
	s_add_i32 s2, s3, s40
	global_load_lds_dwordx4 v[228:229], off
	v_lshl_add_u64 v[228:229], s[0:1], 0, v[132:133]
	s_mov_b32 m0, s2
	v_lshl_add_u64 v[224:225], v[224:225], 0, s[12:13]
	global_load_lds_dwordx4 v[228:229], off
	v_lshl_add_u64 v[228:229], s[0:1], 0, v[136:137]
	s_add_i32 m0, s2, 0x2000
	s_nop 0
	global_load_lds_dwordx4 v[228:229], off
	s_mov_b32 m0, s45
	s_nop 0
	global_load_lds_dwordx4 v[224:225], off
	v_lshl_add_u64 v[224:225], v[226:227], 0, s[12:13]
	s_mov_b32 m0, s46
	s_nop 0
	global_load_lds_dwordx4 v[224:225], off
	s_and_b64 vcc, exec, s[14:15]
	s_cbranch_vccnz .Lwa_1129l_3
	s_waitcnt vmcnt(8)

.Lwb_1129l_3:
	s_setprio 0
	s_barrier
	s_add_i32 s56, s56, 2
	s_add_u32 s54, s54, 0x4000
	s_addc_u32 s55, s55, 0
	s_add_u32 s28, s28, 0x100
	s_addc_u32 s29, s29, 0
	s_cmp_gt_u32 s56, 29
	s_cbranch_scc0 .LBB0_1129
	s_and_b64 vcc, exec, s[14:15]
	s_cbranch_vccz .LBB0_1132
	s_barrier

.LBB0_1152:
	s_ashr_i32 s21, s20, 31
	s_lshl_b64 s[0:1], s[20:21], 20
	s_add_u32 s22, s36, s0
	s_addc_u32 s23, s37, s1
	s_and_b64 s[0:1], s[4:5], exec
	s_cselect_b32 s21, s23, s31
	s_cselect_b32 s52, s22, s30
	s_ashr_i32 s19, s18, 31
	s_lshl_b64 s[0:1], s[18:19], 20
	s_add_u32 s24, s38, s0
	s_addc_u32 s25, s39, s1
	s_and_b64 s[0:1], s[4:5], exec
	s_cselect_b32 s19, s25, s29
	s_cselect_b32 s53, s24, s28
	s_add_u32 s54, s28, 0x4000
	s_addc_u32 s55, s29, 0
	s_add_u32 s28, s30, 0x80080
	s_addc_u32 s29, s31, 0
	s_mov_b32 s56, -2
	ds_read_b128 v[146:149], v1
	ds_read_b128 v[150:153], v1 offset:1024
	ds_read_b128 v[160:163], v1 offset:2048
	ds_read_b128 v[164:167], v1 offset:3072
	ds_read_b128 v[168:171], v154
	ds_read_b128 v[172:175], v154 offset:1024
	ds_read_b128 v[176:179], v154 offset:2048
	ds_read_b128 v[180:183], v154 offset:3072
	s_add_u32 s0, s28, 0xfff80080
	s_addc_u32 s1, s29, -1
	s_cmp_eq_u32 s56, 28
	s_cselect_b32 s35, s21, s1
	s_cselect_b32 s34, s52, s0
	s_cselect_b32 s31, s19, s55
	s_cselect_b32 s30, s53, s54
	v_lshl_add_u64 v[216:217], s[28:29], 0, v[138:139]
	s_add_i32 m0, s27, 0xc000
	ds_read_b128 v[184:187], v155
	ds_read_b128 v[188:191], v155 offset:1024
	ds_read_b128 v[192:195], v155 offset:2048
	ds_read_b128 v[196:199], v155 offset:3072
	ds_read_b128 v[200:203], v155 offset:4096
	ds_read_b128 v[204:207], v155 offset:5120
	ds_read_b128 v[208:211], v155 offset:6144
	ds_read_b128 v[212:215], v155 offset:7168
	global_load_lds_dwordx4 v[216:217], off
	v_lshl_add_u64 v[216:217], s[28:29], 0, v[140:141]
	s_add_i32 m0, s27, 0xe000
	s_nop 0
	global_load_lds_dwordx4 v[216:217], off
	s_and_b64 vcc, exec, s[14:15]
	s_cbranch_vccnz .Lwa_1153p_0
	s_waitcnt vmcnt(8)
.Lwa_1153p_0:
	s_waitcnt lgkmcnt(0)
	s_barrier
	s_setprio 1
	s_waitcnt lgkmcnt(0)
	v_mfma_f32_16x16x32_bf16 v[126:129], v[146:149], v[184:187], 0
	v_mfma_f32_16x16x32_bf16 v[122:125], v[160:163], v[184:187], 0
	v_mfma_f32_16x16x32_bf16 v[110:113], v[146:149], v[192:195], 0
	v_mfma_f32_16x16x32_bf16 v[106:109], v[160:163], v[192:195], 0
	v_mfma_f32_16x16x32_bf16 v[94:97], v[146:149], v[200:203], 0
	v_mfma_f32_16x16x32_bf16 v[90:93], v[160:163], v[200:203], 0
	v_mfma_f32_16x16x32_bf16 v[78:81], v[146:149], v[208:211], 0
	v_mfma_f32_16x16x32_bf16 v[74:77], v[160:163], v[208:211], 0
	v_mfma_f32_16x16x32_bf16 v[126:129], v[150:153], v[188:191], v[126:129]
	v_mfma_f32_16x16x32_bf16 v[122:125], v[164:167], v[188:191], v[122:125]
	v_mfma_f32_16x16x32_bf16 v[110:113], v[150:153], v[196:199], v[110:113]
	v_mfma_f32_16x16x32_bf16 v[106:109], v[164:167], v[196:199], v[106:109]
	v_mfma_f32_16x16x32_bf16 v[94:97], v[150:153], v[204:207], v[94:97]
	v_mfma_f32_16x16x32_bf16 v[90:93], v[164:167], v[204:207], v[90:93]
	v_mfma_f32_16x16x32_bf16 v[78:81], v[150:153], v[212:215], v[78:81]
	v_mfma_f32_16x16x32_bf16 v[74:77], v[164:167], v[212:215], v[74:77]
	s_setprio 0
	s_setprio 1
	v_mfma_f32_16x16x32_bf16 v[118:121], v[168:171], v[184:187], 0
	v_mfma_f32_16x16x32_bf16 v[114:117], v[176:179], v[184:187], 0
	v_mfma_f32_16x16x32_bf16 v[102:105], v[168:171], v[192:195], 0
	v_mfma_f32_16x16x32_bf16 v[98:101], v[176:179], v[192:195], 0
	v_mfma_f32_16x16x32_bf16 v[86:89], v[168:171], v[200:203], 0
	v_mfma_f32_16x16x32_bf16 v[82:85], v[176:179], v[200:203], 0
	v_mfma_f32_16x16x32_bf16 v[70:73], v[168:171], v[208:211], 0
	v_mfma_f32_16x16x32_bf16 v[66:69], v[176:179], v[208:211], 0
	v_mfma_f32_16x16x32_bf16 v[118:121], v[172:175], v[188:191], v[118:121]
	v_mfma_f32_16x16x32_bf16 v[114:117], v[180:183], v[188:191], v[114:117]
	v_mfma_f32_16x16x32_bf16 v[102:105], v[172:175], v[196:199], v[102:105]
	v_mfma_f32_16x16x32_bf16 v[98:101], v[180:183], v[196:199], v[98:101]
	v_mfma_f32_16x16x32_bf16 v[86:89], v[172:175], v[204:207], v[86:89]
	v_mfma_f32_16x16x32_bf16 v[82:85], v[180:183], v[204:207], v[82:85]
	v_mfma_f32_16x16x32_bf16 v[70:73], v[172:175], v[212:215], v[70:73]
	v_mfma_f32_16x16x32_bf16 v[66:69], v[180:183], v[212:215], v[66:69]
	s_cbranch_vccz .Lwb_1153p_0
	s_waitcnt vmcnt(8)
.Lwb_1153p_0:
	s_setprio 0
	s_barrier
	s_add_i32 s0, s48, s40
	v_lshl_add_u64 v[216:217], s[30:31], 0, v[132:133]
	s_mov_b32 m0, s0
	ds_read_b128 v[184:187], v155 offset:16384
	ds_read_b128 v[188:191], v155 offset:17408
	ds_read_b128 v[192:195], v155 offset:18432
	ds_read_b128 v[196:199], v155 offset:19456
	ds_read_b128 v[200:203], v155 offset:20480
	ds_read_b128 v[204:207], v155 offset:21504
	ds_read_b128 v[208:211], v155 offset:22528
	ds_read_b128 v[212:215], v155 offset:23552
	global_load_lds_dwordx4 v[216:217], off
	s_add_i32 m0, s0, 0x2000
	s_add_u32 s0, s30, 0x80000
	v_lshl_add_u64 v[216:217], s[30:31], 0, v[136:137]
	s_addc_u32 s1, s31, 0
	s_add_i32 s2, s49, s40
	global_load_lds_dwordx4 v[216:217], off
	v_lshl_add_u64 v[216:217], s[0:1], 0, v[132:133]
	s_mov_b32 m0, s2
	v_lshl_add_u64 v[218:219], s[34:35], 0, v[134:135]
	global_load_lds_dwordx4 v[216:217], off
	v_lshl_add_u64 v[216:217], s[0:1], 0, v[136:137]
	s_add_i32 m0, s2, 0x2000
	s_nop 0
	global_load_lds_dwordx4 v[216:217], off
	v_lshl_add_u64 v[216:217], s[34:35], 0, v[130:131]
	s_mov_b32 m0, s27
	s_nop 0
	global_load_lds_dwordx4 v[216:217], off
	s_mov_b32 m0, s41
	s_nop 0
	global_load_lds_dwordx4 v[218:219], off
	s_and_b64 vcc, exec, s[14:15]
	s_cbranch_vccnz .Lwa_1153p_1
	s_waitcnt vmcnt(8)
.Lwa_1153p_1:
	s_waitcnt lgkmcnt(0)
	s_barrier
	s_setprio 1
	s_waitcnt lgkmcnt(0)
	v_mfma_f32_16x16x32_bf16 v[62:65], v[146:149], v[184:187], 0
	v_mfma_f32_16x16x32_bf16 v[58:61], v[160:163], v[184:187], 0
	v_mfma_f32_16x16x32_bf16 v[46:49], v[146:149], v[192:195], 0
	v_mfma_f32_16x16x32_bf16 v[42:45], v[160:163], v[192:195], 0
	v_mfma_f32_16x16x32_bf16 v[30:33], v[146:149], v[200:203], 0
	v_mfma_f32_16x16x32_bf16 v[26:29], v[160:163], v[200:203], 0
	v_mfma_f32_16x16x32_bf16 v[14:17], v[146:149], v[208:211], 0
	v_mfma_f32_16x16x32_bf16 v[10:13], v[160:163], v[208:211], 0
	v_mfma_f32_16x16x32_bf16 v[62:65], v[150:153], v[188:191], v[62:65]
	v_mfma_f32_16x16x32_bf16 v[58:61], v[164:167], v[188:191], v[58:61]
	v_mfma_f32_16x16x32_bf16 v[46:49], v[150:153], v[196:199], v[46:49]
	v_mfma_f32_16x16x32_bf16 v[42:45], v[164:167], v[196:199], v[42:45]
	v_mfma_f32_16x16x32_bf16 v[30:33], v[150:153], v[204:207], v[30:33]
	v_mfma_f32_16x16x32_bf16 v[26:29], v[164:167], v[204:207], v[26:29]
	v_mfma_f32_16x16x32_bf16 v[14:17], v[150:153], v[212:215], v[14:17]
	v_mfma_f32_16x16x32_bf16 v[10:13], v[164:167], v[212:215], v[10:13]
	s_setprio 0
	s_setprio 1
	v_mfma_f32_16x16x32_bf16 v[54:57], v[168:171], v[184:187], 0
	v_mfma_f32_16x16x32_bf16 v[50:53], v[176:179], v[184:187], 0
	v_mfma_f32_16x16x32_bf16 v[38:41], v[168:171], v[192:195], 0
	v_mfma_f32_16x16x32_bf16 v[34:37], v[176:179], v[192:195], 0
	v_mfma_f32_16x16x32_bf16 v[22:25], v[168:171], v[200:203], 0
	v_mfma_f32_16x16x32_bf16 v[18:21], v[176:179], v[200:203], 0
	v_mfma_f32_16x16x32_bf16 v[6:9], v[168:171], v[208:211], 0
	v_mfma_f32_16x16x32_bf16 v[2:5], v[176:179], v[208:211], 0
	v_mfma_f32_16x16x32_bf16 v[54:57], v[172:175], v[188:191], v[54:57]
	v_mfma_f32_16x16x32_bf16 v[50:53], v[180:183], v[188:191], v[50:53]
	v_mfma_f32_16x16x32_bf16 v[38:41], v[172:175], v[196:199], v[38:41]
	v_mfma_f32_16x16x32_bf16 v[34:37], v[180:183], v[196:199], v[34:37]
	v_mfma_f32_16x16x32_bf16 v[22:25], v[172:175], v[204:207], v[22:25]
	v_mfma_f32_16x16x32_bf16 v[18:21], v[180:183], v[204:207], v[18:21]
	v_mfma_f32_16x16x32_bf16 v[6:9], v[172:175], v[212:215], v[6:9]
	v_mfma_f32_16x16x32_bf16 v[2:5], v[180:183], v[212:215], v[2:5]
	s_cbranch_vccz .Lwb_1153p_1
	s_waitcnt vmcnt(8)

.LBB0_1153:
	ds_read_b128 v[146:149], v1
	ds_read_b128 v[150:153], v1 offset:1024
	ds_read_b128 v[160:163], v1 offset:2048
	ds_read_b128 v[164:167], v1 offset:3072
	ds_read_b128 v[168:171], v154
	ds_read_b128 v[172:175], v154 offset:1024
	ds_read_b128 v[176:179], v154 offset:2048
	ds_read_b128 v[180:183], v154 offset:3072
	s_add_u32 s0, s28, 0xfff80080
	s_addc_u32 s1, s29, -1
	s_cmp_eq_u32 s56, 28
	s_cselect_b32 s35, s21, s1
	s_cselect_b32 s34, s52, s0
	s_cselect_b32 s31, s19, s55
	s_cselect_b32 s30, s53, s54
	v_lshl_add_u64 v[216:217], s[28:29], 0, v[138:139]
	s_add_i32 m0, s27, 0xc000
	ds_read_b128 v[184:187], v155
	ds_read_b128 v[188:191], v155 offset:1024
	ds_read_b128 v[192:195], v155 offset:2048
	ds_read_b128 v[196:199], v155 offset:3072
	ds_read_b128 v[200:203], v155 offset:4096
	ds_read_b128 v[204:207], v155 offset:5120
	ds_read_b128 v[208:211], v155 offset:6144
	ds_read_b128 v[212:215], v155 offset:7168
	global_load_lds_dwordx4 v[216:217], off
	v_lshl_add_u64 v[216:217], s[28:29], 0, v[140:141]
	s_add_i32 m0, s27, 0xe000
	s_nop 0
	global_load_lds_dwordx4 v[216:217], off
	s_and_b64 vcc, exec, s[14:15]
	s_cbranch_vccnz .Lwa_1153l_0
	s_waitcnt vmcnt(8)
.Lwa_1153l_0:
	s_waitcnt lgkmcnt(0)
	s_barrier
	s_setprio 1
	s_waitcnt lgkmcnt(0)
	v_mfma_f32_16x16x32_bf16 v[126:129], v[146:149], v[184:187], v[126:129]
	v_mfma_f32_16x16x32_bf16 v[122:125], v[160:163], v[184:187], v[122:125]
	v_mfma_f32_16x16x32_bf16 v[110:113], v[146:149], v[192:195], v[110:113]
	v_mfma_f32_16x16x32_bf16 v[106:109], v[160:163], v[192:195], v[106:109]
	v_mfma_f32_16x16x32_bf16 v[94:97], v[146:149], v[200:203], v[94:97]
	v_mfma_f32_16x16x32_bf16 v[90:93], v[160:163], v[200:203], v[90:93]
	v_mfma_f32_16x16x32_bf16 v[78:81], v[146:149], v[208:211], v[78:81]
	v_mfma_f32_16x16x32_bf16 v[74:77], v[160:163], v[208:211], v[74:77]
	v_mfma_f32_16x16x32_bf16 v[126:129], v[150:153], v[188:191], v[126:129]
	v_mfma_f32_16x16x32_bf16 v[122:125], v[164:167], v[188:191], v[122:125]
	v_mfma_f32_16x16x32_bf16 v[110:113], v[150:153], v[196:199], v[110:113]
	v_mfma_f32_16x16x32_bf16 v[106:109], v[164:167], v[196:199], v[106:109]
	v_mfma_f32_16x16x32_bf16 v[94:97], v[150:153], v[204:207], v[94:97]
	v_mfma_f32_16x16x32_bf16 v[90:93], v[164:167], v[204:207], v[90:93]
	v_mfma_f32_16x16x32_bf16 v[78:81], v[150:153], v[212:215], v[78:81]
	v_mfma_f32_16x16x32_bf16 v[74:77], v[164:167], v[212:215], v[74:77]
	s_setprio 0
	s_setprio 1
	v_mfma_f32_16x16x32_bf16 v[118:121], v[168:171], v[184:187], v[118:121]
	v_mfma_f32_16x16x32_bf16 v[114:117], v[176:179], v[184:187], v[114:117]
	v_mfma_f32_16x16x32_bf16 v[102:105], v[168:171], v[192:195], v[102:105]
	v_mfma_f32_16x16x32_bf16 v[98:101], v[176:179], v[192:195], v[98:101]
	v_mfma_f32_16x16x32_bf16 v[86:89], v[168:171], v[200:203], v[86:89]
	v_mfma_f32_16x16x32_bf16 v[82:85], v[176:179], v[200:203], v[82:85]
	v_mfma_f32_16x16x32_bf16 v[70:73], v[168:171], v[208:211], v[70:73]
	v_mfma_f32_16x16x32_bf16 v[66:69], v[176:179], v[208:211], v[66:69]
	v_mfma_f32_16x16x32_bf16 v[118:121], v[172:175], v[188:191], v[118:121]
	v_mfma_f32_16x16x32_bf16 v[114:117], v[180:183], v[188:191], v[114:117]
	v_mfma_f32_16x16x32_bf16 v[102:105], v[172:175], v[196:199], v[102:105]
	v_mfma_f32_16x16x32_bf16 v[98:101], v[180:183], v[196:199], v[98:101]
	v_mfma_f32_16x16x32_bf16 v[86:89], v[172:175], v[204:207], v[86:89]
	v_mfma_f32_16x16x32_bf16 v[82:85], v[180:183], v[204:207], v[82:85]
	v_mfma_f32_16x16x32_bf16 v[70:73], v[172:175], v[212:215], v[70:73]
	v_mfma_f32_16x16x32_bf16 v[66:69], v[180:183], v[212:215], v[66:69]
	s_cbranch_vccz .Lwb_1153l_0
	s_waitcnt vmcnt(8)

.Lwa_1153l_1:
	s_waitcnt lgkmcnt(0)
	s_barrier
	s_setprio 1
	s_waitcnt lgkmcnt(0)
	v_mfma_f32_16x16x32_bf16 v[62:65], v[146:149], v[184:187], v[62:65]
	v_mfma_f32_16x16x32_bf16 v[58:61], v[160:163], v[184:187], v[58:61]
	v_mfma_f32_16x16x32_bf16 v[46:49], v[146:149], v[192:195], v[46:49]
	v_mfma_f32_16x16x32_bf16 v[42:45], v[160:163], v[192:195], v[42:45]
	v_mfma_f32_16x16x32_bf16 v[30:33], v[146:149], v[200:203], v[30:33]
	v_mfma_f32_16x16x32_bf16 v[26:29], v[160:163], v[200:203], v[26:29]
	v_mfma_f32_16x16x32_bf16 v[14:17], v[146:149], v[208:211], v[14:17]
	v_mfma_f32_16x16x32_bf16 v[10:13], v[160:163], v[208:211], v[10:13]
	v_mfma_f32_16x16x32_bf16 v[62:65], v[150:153], v[188:191], v[62:65]
	v_mfma_f32_16x16x32_bf16 v[58:61], v[164:167], v[188:191], v[58:61]
	v_mfma_f32_16x16x32_bf16 v[46:49], v[150:153], v[196:199], v[46:49]
	v_mfma_f32_16x16x32_bf16 v[42:45], v[164:167], v[196:199], v[42:45]
	v_mfma_f32_16x16x32_bf16 v[30:33], v[150:153], v[204:207], v[30:33]
	v_mfma_f32_16x16x32_bf16 v[26:29], v[164:167], v[204:207], v[26:29]
	v_mfma_f32_16x16x32_bf16 v[14:17], v[150:153], v[212:215], v[14:17]
	v_mfma_f32_16x16x32_bf16 v[10:13], v[164:167], v[212:215], v[10:13]
	s_setprio 0
	s_setprio 1
	v_mfma_f32_16x16x32_bf16 v[54:57], v[168:171], v[184:187], v[54:57]
	v_mfma_f32_16x16x32_bf16 v[50:53], v[176:179], v[184:187], v[50:53]
	v_mfma_f32_16x16x32_bf16 v[38:41], v[168:171], v[192:195], v[38:41]
	v_mfma_f32_16x16x32_bf16 v[34:37], v[176:179], v[192:195], v[34:37]
	v_mfma_f32_16x16x32_bf16 v[22:25], v[168:171], v[200:203], v[22:25]
	v_mfma_f32_16x16x32_bf16 v[18:21], v[176:179], v[200:203], v[18:21]
	v_mfma_f32_16x16x32_bf16 v[6:9], v[168:171], v[208:211], v[6:9]
	v_mfma_f32_16x16x32_bf16 v[2:5], v[176:179], v[208:211], v[2:5]
	v_mfma_f32_16x16x32_bf16 v[54:57], v[172:175], v[188:191], v[54:57]
	v_mfma_f32_16x16x32_bf16 v[50:53], v[180:183], v[188:191], v[50:53]
	v_mfma_f32_16x16x32_bf16 v[38:41], v[172:175], v[196:199], v[38:41]
	v_mfma_f32_16x16x32_bf16 v[34:37], v[180:183], v[196:199], v[34:37]
	v_mfma_f32_16x16x32_bf16 v[22:25], v[172:175], v[204:207], v[22:25]
	v_mfma_f32_16x16x32_bf16 v[18:21], v[180:183], v[204:207], v[18:21]
	v_mfma_f32_16x16x32_bf16 v[6:9], v[172:175], v[212:215], v[6:9]
	v_mfma_f32_16x16x32_bf16 v[2:5], v[180:183], v[212:215], v[2:5]
	s_cbranch_vccz .Lwb_1153l_1
	s_waitcnt vmcnt(8)

.Lmid_1153:
	s_add_i32 s2, 0, 0x18000
	v_add_u32_e32 v0, s2, v159
	s_add_i32 s3, 0, 0x1c000
	ds_read_b128 v[146:149], v0
	ds_read_b128 v[150:153], v0 offset:1024
	ds_read_b128 v[160:163], v0 offset:2048
	ds_read_b128 v[164:167], v0 offset:3072
	v_add_u32_e32 v0, s3, v159
	ds_read_b128 v[168:171], v0
	ds_read_b128 v[172:175], v0 offset:1024
	ds_read_b128 v[176:179], v0 offset:2048
	ds_read_b128 v[180:183], v0 offset:3072
	s_add_u32 s0, s34, 0x80000
	s_addc_u32 s1, s35, 0
	s_mov_b32 m0, s42
	v_lshl_add_u64 v[220:221], s[0:1], 0, v[130:131]
	ds_read_b128 v[184:187], v155 offset:32768
	ds_read_b128 v[188:191], v155 offset:33792
	ds_read_b128 v[192:195], v155 offset:34816
	ds_read_b128 v[196:199], v155 offset:35840
	ds_read_b128 v[200:203], v155 offset:36864
	ds_read_b128 v[204:207], v155 offset:37888
	ds_read_b128 v[208:211], v155 offset:38912
	ds_read_b128 v[212:215], v155 offset:39936
	global_load_lds_dwordx4 v[220:221], off
	v_lshl_add_u64 v[220:221], s[0:1], 0, v[134:135]
	s_mov_b32 m0, s43
	s_nop 0
	global_load_lds_dwordx4 v[220:221], off
	s_and_b64 vcc, exec, s[14:15]
	s_cbranch_vccnz .Lwa_1153l_2
	s_waitcnt vmcnt(8)

.Lwb_1153l_2:
	s_setprio 0
	s_barrier
	s_add_u32 s0, s30, 0x2000
	s_addc_u32 s1, s31, 0
	s_add_i32 s2, s2, s40
	v_lshl_add_u64 v[220:221], s[0:1], 0, v[132:133]
	s_mov_b32 m0, s2
	ds_read_b128 v[184:187], v155 offset:49152
	ds_read_b128 v[188:191], v155 offset:50176
	ds_read_b128 v[192:195], v155 offset:51200
	ds_read_b128 v[196:199], v155 offset:52224
	ds_read_b128 v[200:203], v155 offset:53248
	ds_read_b128 v[204:207], v155 offset:54272
	ds_read_b128 v[208:211], v155 offset:55296
	ds_read_b128 v[212:215], v155 offset:56320
	global_load_lds_dwordx4 v[220:221], off
	s_add_i32 m0, s2, 0x2000
	v_lshl_add_u64 v[220:221], s[0:1], 0, v[136:137]
	s_add_u32 s0, s30, 0x82000
	s_addc_u32 s1, s31, 0
	s_add_i32 s2, s3, s40
	global_load_lds_dwordx4 v[220:221], off
	v_lshl_add_u64 v[220:221], s[0:1], 0, v[132:133]
	s_mov_b32 m0, s2
	v_lshl_add_u64 v[216:217], v[216:217], 0, s[12:13]
	global_load_lds_dwordx4 v[220:221], off
	v_lshl_add_u64 v[220:221], s[0:1], 0, v[136:137]
	s_add_i32 m0, s2, 0x2000
	s_nop 0
	global_load_lds_dwordx4 v[220:221], off
	s_mov_b32 m0, s45
	s_nop 0
	global_load_lds_dwordx4 v[216:217], off
	v_lshl_add_u64 v[216:217], v[218:219], 0, s[12:13]
	s_mov_b32 m0, s46
	s_nop 0
	global_load_lds_dwordx4 v[216:217], off
	s_and_b64 vcc, exec, s[14:15]
	s_cbranch_vccnz .Lwa_1153l_3
	s_waitcnt vmcnt(8)

.LBB0_1227:
	s_ashr_i32 s27, s26, 31
	s_lshl_b64 s[0:1], s[26:27], 20
	s_add_u32 s28, s42, s0
	s_addc_u32 s29, s43, s1
	s_and_b64 s[0:1], s[4:5], exec
	s_cselect_b32 s27, s29, s39
	s_cselect_b32 s57, s28, s38
	s_ashr_i32 s25, s24, 31
	s_lshl_b64 s[0:1], s[24:25], 20
	s_add_u32 s30, s44, s0
	s_addc_u32 s31, s45, s1
	s_and_b64 s[0:1], s[4:5], exec
	s_cselect_b32 s25, s31, s37
	s_cselect_b32 s58, s30, s36
	s_add_u32 s59, s36, 0x4000
	s_addc_u32 s60, s37, 0
	s_add_u32 s36, s38, 0x80080
	s_addc_u32 s37, s39, 0
	s_mov_b32 s61, -2
	ds_read_b128 v[146:149], v154
	ds_read_b128 v[158:161], v154 offset:1024
	ds_read_b128 v[162:165], v154 offset:2048
	ds_read_b128 v[166:169], v154 offset:3072
	ds_read_b128 v[170:173], v155
	ds_read_b128 v[174:177], v155 offset:1024
	ds_read_b128 v[178:181], v155 offset:2048
	ds_read_b128 v[182:185], v155 offset:3072
	s_add_u32 s0, s36, 0xfff80080
	s_addc_u32 s1, s37, -1
	s_cmp_eq_u32 s61, 28
	s_cselect_b32 s41, s27, s1
	s_cselect_b32 s40, s57, s0
	s_cselect_b32 s39, s25, s60
	s_cselect_b32 s38, s58, s59
	v_lshl_add_u64 v[150:151], s[36:37], 0, v[138:139]
	s_add_i32 m0, s35, 0xc000
	ds_read_b128 v[186:189], v156
	ds_read_b128 v[190:193], v156 offset:1024
	ds_read_b128 v[194:197], v156 offset:2048
	ds_read_b128 v[198:201], v156 offset:3072
	ds_read_b128 v[202:205], v156 offset:4096
	ds_read_b128 v[206:209], v156 offset:5120
	ds_read_b128 v[210:213], v156 offset:6144
	ds_read_b128 v[214:217], v156 offset:7168
	global_load_lds_dwordx4 v[150:151], off
	v_lshl_add_u64 v[150:151], s[36:37], 0, v[140:141]
	s_add_i32 m0, s35, 0xe000
	s_nop 0
	global_load_lds_dwordx4 v[150:151], off
	s_and_b64 vcc, exec, s[14:15]
	s_cbranch_vccnz .Lwa_1228p_0
	s_waitcnt vmcnt(8)
.Lwa_1228p_0:
	s_waitcnt lgkmcnt(0)
	s_barrier
	s_setprio 1
	s_waitcnt lgkmcnt(0)
	v_mfma_f32_16x16x32_bf16 v[126:129], v[146:149], v[186:189], 0
	v_mfma_f32_16x16x32_bf16 v[122:125], v[162:165], v[186:189], 0
	v_mfma_f32_16x16x32_bf16 v[110:113], v[146:149], v[194:197], 0
	v_mfma_f32_16x16x32_bf16 v[106:109], v[162:165], v[194:197], 0
	v_mfma_f32_16x16x32_bf16 v[94:97], v[146:149], v[202:205], 0
	v_mfma_f32_16x16x32_bf16 v[90:93], v[162:165], v[202:205], 0
	v_mfma_f32_16x16x32_bf16 v[78:81], v[146:149], v[210:213], 0
	v_mfma_f32_16x16x32_bf16 v[74:77], v[162:165], v[210:213], 0
	v_mfma_f32_16x16x32_bf16 v[126:129], v[158:161], v[190:193], v[126:129]
	v_mfma_f32_16x16x32_bf16 v[122:125], v[166:169], v[190:193], v[122:125]
	v_mfma_f32_16x16x32_bf16 v[110:113], v[158:161], v[198:201], v[110:113]
	v_mfma_f32_16x16x32_bf16 v[106:109], v[166:169], v[198:201], v[106:109]
	v_mfma_f32_16x16x32_bf16 v[94:97], v[158:161], v[206:209], v[94:97]
	v_mfma_f32_16x16x32_bf16 v[90:93], v[166:169], v[206:209], v[90:93]
	v_mfma_f32_16x16x32_bf16 v[78:81], v[158:161], v[214:217], v[78:81]
	v_mfma_f32_16x16x32_bf16 v[74:77], v[166:169], v[214:217], v[74:77]
	s_setprio 0
	s_setprio 1
	v_mfma_f32_16x16x32_bf16 v[118:121], v[170:173], v[186:189], 0
	v_mfma_f32_16x16x32_bf16 v[114:117], v[178:181], v[186:189], 0
	v_mfma_f32_16x16x32_bf16 v[102:105], v[170:173], v[194:197], 0
	v_mfma_f32_16x16x32_bf16 v[98:101], v[178:181], v[194:197], 0
	v_mfma_f32_16x16x32_bf16 v[86:89], v[170:173], v[202:205], 0
	v_mfma_f32_16x16x32_bf16 v[82:85], v[178:181], v[202:205], 0
	v_mfma_f32_16x16x32_bf16 v[70:73], v[170:173], v[210:213], 0
	v_mfma_f32_16x16x32_bf16 v[66:69], v[178:181], v[210:213], 0
	v_mfma_f32_16x16x32_bf16 v[118:121], v[174:177], v[190:193], v[118:121]
	v_mfma_f32_16x16x32_bf16 v[114:117], v[182:185], v[190:193], v[114:117]
	v_mfma_f32_16x16x32_bf16 v[102:105], v[174:177], v[198:201], v[102:105]
	v_mfma_f32_16x16x32_bf16 v[98:101], v[182:185], v[198:201], v[98:101]
	v_mfma_f32_16x16x32_bf16 v[86:89], v[174:177], v[206:209], v[86:89]
	v_mfma_f32_16x16x32_bf16 v[82:85], v[182:185], v[206:209], v[82:85]
	v_mfma_f32_16x16x32_bf16 v[70:73], v[174:177], v[214:217], v[70:73]
	v_mfma_f32_16x16x32_bf16 v[66:69], v[182:185], v[214:217], v[66:69]
	s_cbranch_vccz .Lwb_1228p_0
	s_waitcnt vmcnt(8)
.Lwb_1228p_0:
	s_setprio 0
	s_barrier
	s_add_i32 s0, s54, s46
	v_lshl_add_u64 v[150:151], s[38:39], 0, v[132:133]
	s_mov_b32 m0, s0
	ds_read_b128 v[186:189], v156 offset:16384
	ds_read_b128 v[190:193], v156 offset:17408
	ds_read_b128 v[194:197], v156 offset:18432
	ds_read_b128 v[198:201], v156 offset:19456
	ds_read_b128 v[202:205], v156 offset:20480
	ds_read_b128 v[206:209], v156 offset:21504
	ds_read_b128 v[210:213], v156 offset:22528
	ds_read_b128 v[214:217], v156 offset:23552
	global_load_lds_dwordx4 v[150:151], off
	s_add_i32 m0, s0, 0x2000
	s_add_u32 s0, s38, 0x80000
	v_lshl_add_u64 v[150:151], s[38:39], 0, v[136:137]
	s_addc_u32 s1, s39, 0
	s_add_i32 s2, s55, s46
	global_load_lds_dwordx4 v[150:151], off
	v_lshl_add_u64 v[150:151], s[0:1], 0, v[132:133]
	s_mov_b32 m0, s2
	v_lshl_add_u64 v[218:219], s[40:41], 0, v[134:135]
	global_load_lds_dwordx4 v[150:151], off
	v_lshl_add_u64 v[150:151], s[0:1], 0, v[136:137]
	s_add_i32 m0, s2, 0x2000
	s_nop 0
	global_load_lds_dwordx4 v[150:151], off
	v_lshl_add_u64 v[150:151], s[40:41], 0, v[130:131]
	s_mov_b32 m0, s35
	s_nop 0
	global_load_lds_dwordx4 v[150:151], off
	s_mov_b32 m0, s47
	s_nop 0
	global_load_lds_dwordx4 v[218:219], off
	s_and_b64 vcc, exec, s[14:15]
	s_cbranch_vccnz .Lwa_1228p_1
	s_waitcnt vmcnt(8)
.Lwa_1228p_1:
	s_waitcnt lgkmcnt(0)
	s_barrier
	s_setprio 1
	s_waitcnt lgkmcnt(0)
	v_mfma_f32_16x16x32_bf16 v[62:65], v[146:149], v[186:189], 0
	v_mfma_f32_16x16x32_bf16 v[58:61], v[162:165], v[186:189], 0
	v_mfma_f32_16x16x32_bf16 v[46:49], v[146:149], v[194:197], 0
	v_mfma_f32_16x16x32_bf16 v[42:45], v[162:165], v[194:197], 0
	v_mfma_f32_16x16x32_bf16 v[30:33], v[146:149], v[202:205], 0
	v_mfma_f32_16x16x32_bf16 v[26:29], v[162:165], v[202:205], 0
	v_mfma_f32_16x16x32_bf16 v[14:17], v[146:149], v[210:213], 0
	v_mfma_f32_16x16x32_bf16 v[10:13], v[162:165], v[210:213], 0
	v_mfma_f32_16x16x32_bf16 v[62:65], v[158:161], v[190:193], v[62:65]
	v_mfma_f32_16x16x32_bf16 v[58:61], v[166:169], v[190:193], v[58:61]
	v_mfma_f32_16x16x32_bf16 v[46:49], v[158:161], v[198:201], v[46:49]
	v_mfma_f32_16x16x32_bf16 v[42:45], v[166:169], v[198:201], v[42:45]
	v_mfma_f32_16x16x32_bf16 v[30:33], v[158:161], v[206:209], v[30:33]
	v_mfma_f32_16x16x32_bf16 v[26:29], v[166:169], v[206:209], v[26:29]
	v_mfma_f32_16x16x32_bf16 v[14:17], v[158:161], v[214:217], v[14:17]
	v_mfma_f32_16x16x32_bf16 v[10:13], v[166:169], v[214:217], v[10:13]
	s_setprio 0
	s_setprio 1
	v_mfma_f32_16x16x32_bf16 v[54:57], v[170:173], v[186:189], 0
	v_mfma_f32_16x16x32_bf16 v[50:53], v[178:181], v[186:189], 0
	v_mfma_f32_16x16x32_bf16 v[38:41], v[170:173], v[194:197], 0
	v_mfma_f32_16x16x32_bf16 v[34:37], v[178:181], v[194:197], 0
	v_mfma_f32_16x16x32_bf16 v[22:25], v[170:173], v[202:205], 0
	v_mfma_f32_16x16x32_bf16 v[18:21], v[178:181], v[202:205], 0
	v_mfma_f32_16x16x32_bf16 v[6:9], v[170:173], v[210:213], 0
	v_mfma_f32_16x16x32_bf16 v[2:5], v[178:181], v[210:213], 0
	v_mfma_f32_16x16x32_bf16 v[54:57], v[174:177], v[190:193], v[54:57]
	v_mfma_f32_16x16x32_bf16 v[50:53], v[182:185], v[190:193], v[50:53]
	v_mfma_f32_16x16x32_bf16 v[38:41], v[174:177], v[198:201], v[38:41]
	v_mfma_f32_16x16x32_bf16 v[34:37], v[182:185], v[198:201], v[34:37]
	v_mfma_f32_16x16x32_bf16 v[22:25], v[174:177], v[206:209], v[22:25]
	v_mfma_f32_16x16x32_bf16 v[18:21], v[182:185], v[206:209], v[18:21]
	v_mfma_f32_16x16x32_bf16 v[6:9], v[174:177], v[214:217], v[6:9]
	v_mfma_f32_16x16x32_bf16 v[2:5], v[182:185], v[214:217], v[2:5]
	s_cbranch_vccz .Lwb_1228p_1
	s_waitcnt vmcnt(8)

.LBB0_1228:
	ds_read_b128 v[146:149], v154
	ds_read_b128 v[158:161], v154 offset:1024
	ds_read_b128 v[162:165], v154 offset:2048
	ds_read_b128 v[166:169], v154 offset:3072
	ds_read_b128 v[170:173], v155
	ds_read_b128 v[174:177], v155 offset:1024
	ds_read_b128 v[178:181], v155 offset:2048
	ds_read_b128 v[182:185], v155 offset:3072
	s_add_u32 s0, s36, 0xfff80080
	s_addc_u32 s1, s37, -1
	s_cmp_eq_u32 s61, 28
	s_cselect_b32 s41, s27, s1
	s_cselect_b32 s40, s57, s0
	s_cselect_b32 s39, s25, s60
	s_cselect_b32 s38, s58, s59
	v_lshl_add_u64 v[150:151], s[36:37], 0, v[138:139]
	s_add_i32 m0, s35, 0xc000
	ds_read_b128 v[186:189], v156
	ds_read_b128 v[190:193], v156 offset:1024
	ds_read_b128 v[194:197], v156 offset:2048
	ds_read_b128 v[198:201], v156 offset:3072
	ds_read_b128 v[202:205], v156 offset:4096
	ds_read_b128 v[206:209], v156 offset:5120
	ds_read_b128 v[210:213], v156 offset:6144
	ds_read_b128 v[214:217], v156 offset:7168
	global_load_lds_dwordx4 v[150:151], off
	v_lshl_add_u64 v[150:151], s[36:37], 0, v[140:141]
	s_add_i32 m0, s35, 0xe000
	s_nop 0
	global_load_lds_dwordx4 v[150:151], off
	s_and_b64 vcc, exec, s[14:15]
	s_cbranch_vccnz .Lwa_1228l_0
	s_waitcnt vmcnt(8)
.Lwa_1228l_0:
	s_waitcnt lgkmcnt(0)
	s_barrier
	s_setprio 1
	s_waitcnt lgkmcnt(0)
	v_mfma_f32_16x16x32_bf16 v[126:129], v[146:149], v[186:189], v[126:129]
	v_mfma_f32_16x16x32_bf16 v[122:125], v[162:165], v[186:189], v[122:125]
	v_mfma_f32_16x16x32_bf16 v[110:113], v[146:149], v[194:197], v[110:113]
	v_mfma_f32_16x16x32_bf16 v[106:109], v[162:165], v[194:197], v[106:109]
	v_mfma_f32_16x16x32_bf16 v[94:97], v[146:149], v[202:205], v[94:97]
	v_mfma_f32_16x16x32_bf16 v[90:93], v[162:165], v[202:205], v[90:93]
	v_mfma_f32_16x16x32_bf16 v[78:81], v[146:149], v[210:213], v[78:81]
	v_mfma_f32_16x16x32_bf16 v[74:77], v[162:165], v[210:213], v[74:77]
	v_mfma_f32_16x16x32_bf16 v[126:129], v[158:161], v[190:193], v[126:129]
	v_mfma_f32_16x16x32_bf16 v[122:125], v[166:169], v[190:193], v[122:125]
	v_mfma_f32_16x16x32_bf16 v[110:113], v[158:161], v[198:201], v[110:113]
	v_mfma_f32_16x16x32_bf16 v[106:109], v[166:169], v[198:201], v[106:109]
	v_mfma_f32_16x16x32_bf16 v[94:97], v[158:161], v[206:209], v[94:97]
	v_mfma_f32_16x16x32_bf16 v[90:93], v[166:169], v[206:209], v[90:93]
	v_mfma_f32_16x16x32_bf16 v[78:81], v[158:161], v[214:217], v[78:81]
	v_mfma_f32_16x16x32_bf16 v[74:77], v[166:169], v[214:217], v[74:77]
	s_setprio 0
	s_setprio 1
	v_mfma_f32_16x16x32_bf16 v[118:121], v[170:173], v[186:189], v[118:121]
	v_mfma_f32_16x16x32_bf16 v[114:117], v[178:181], v[186:189], v[114:117]
	v_mfma_f32_16x16x32_bf16 v[102:105], v[170:173], v[194:197], v[102:105]
	v_mfma_f32_16x16x32_bf16 v[98:101], v[178:181], v[194:197], v[98:101]
	v_mfma_f32_16x16x32_bf16 v[86:89], v[170:173], v[202:205], v[86:89]
	v_mfma_f32_16x16x32_bf16 v[82:85], v[178:181], v[202:205], v[82:85]
	v_mfma_f32_16x16x32_bf16 v[70:73], v[170:173], v[210:213], v[70:73]
	v_mfma_f32_16x16x32_bf16 v[66:69], v[178:181], v[210:213], v[66:69]
	v_mfma_f32_16x16x32_bf16 v[118:121], v[174:177], v[190:193], v[118:121]
	v_mfma_f32_16x16x32_bf16 v[114:117], v[182:185], v[190:193], v[114:117]
	v_mfma_f32_16x16x32_bf16 v[102:105], v[174:177], v[198:201], v[102:105]
	v_mfma_f32_16x16x32_bf16 v[98:101], v[182:185], v[198:201], v[98:101]
	v_mfma_f32_16x16x32_bf16 v[86:89], v[174:177], v[206:209], v[86:89]
	v_mfma_f32_16x16x32_bf16 v[82:85], v[182:185], v[206:209], v[82:85]
	v_mfma_f32_16x16x32_bf16 v[70:73], v[174:177], v[214:217], v[70:73]
	v_mfma_f32_16x16x32_bf16 v[66:69], v[182:185], v[214:217], v[66:69]
	s_cbranch_vccz .Lwb_1228l_0
	s_waitcnt vmcnt(8)

.Lwa_1228l_1:
	s_waitcnt lgkmcnt(0)
	s_barrier
	s_setprio 1
	s_waitcnt lgkmcnt(0)
	v_mfma_f32_16x16x32_bf16 v[62:65], v[146:149], v[186:189], v[62:65]
	v_mfma_f32_16x16x32_bf16 v[58:61], v[162:165], v[186:189], v[58:61]
	v_mfma_f32_16x16x32_bf16 v[46:49], v[146:149], v[194:197], v[46:49]
	v_mfma_f32_16x16x32_bf16 v[42:45], v[162:165], v[194:197], v[42:45]
	v_mfma_f32_16x16x32_bf16 v[30:33], v[146:149], v[202:205], v[30:33]
	v_mfma_f32_16x16x32_bf16 v[26:29], v[162:165], v[202:205], v[26:29]
	v_mfma_f32_16x16x32_bf16 v[14:17], v[146:149], v[210:213], v[14:17]
	v_mfma_f32_16x16x32_bf16 v[10:13], v[162:165], v[210:213], v[10:13]
	v_mfma_f32_16x16x32_bf16 v[62:65], v[158:161], v[190:193], v[62:65]
	v_mfma_f32_16x16x32_bf16 v[58:61], v[166:169], v[190:193], v[58:61]
	v_mfma_f32_16x16x32_bf16 v[46:49], v[158:161], v[198:201], v[46:49]
	v_mfma_f32_16x16x32_bf16 v[42:45], v[166:169], v[198:201], v[42:45]
	v_mfma_f32_16x16x32_bf16 v[30:33], v[158:161], v[206:209], v[30:33]
	v_mfma_f32_16x16x32_bf16 v[26:29], v[166:169], v[206:209], v[26:29]
	v_mfma_f32_16x16x32_bf16 v[14:17], v[158:161], v[214:217], v[14:17]
	v_mfma_f32_16x16x32_bf16 v[10:13], v[166:169], v[214:217], v[10:13]
	s_setprio 0
	s_setprio 1
	v_mfma_f32_16x16x32_bf16 v[54:57], v[170:173], v[186:189], v[54:57]
	v_mfma_f32_16x16x32_bf16 v[50:53], v[178:181], v[186:189], v[50:53]
	v_mfma_f32_16x16x32_bf16 v[38:41], v[170:173], v[194:197], v[38:41]
	v_mfma_f32_16x16x32_bf16 v[34:37], v[178:181], v[194:197], v[34:37]
	v_mfma_f32_16x16x32_bf16 v[22:25], v[170:173], v[202:205], v[22:25]
	v_mfma_f32_16x16x32_bf16 v[18:21], v[178:181], v[202:205], v[18:21]
	v_mfma_f32_16x16x32_bf16 v[6:9], v[170:173], v[210:213], v[6:9]
	v_mfma_f32_16x16x32_bf16 v[2:5], v[178:181], v[210:213], v[2:5]
	v_mfma_f32_16x16x32_bf16 v[54:57], v[174:177], v[190:193], v[54:57]
	v_mfma_f32_16x16x32_bf16 v[50:53], v[182:185], v[190:193], v[50:53]
	v_mfma_f32_16x16x32_bf16 v[38:41], v[174:177], v[198:201], v[38:41]
	v_mfma_f32_16x16x32_bf16 v[34:37], v[182:185], v[198:201], v[34:37]
	v_mfma_f32_16x16x32_bf16 v[22:25], v[174:177], v[206:209], v[22:25]
	v_mfma_f32_16x16x32_bf16 v[18:21], v[182:185], v[206:209], v[18:21]
	v_mfma_f32_16x16x32_bf16 v[6:9], v[174:177], v[214:217], v[6:9]
	v_mfma_f32_16x16x32_bf16 v[2:5], v[182:185], v[214:217], v[2:5]
	s_cbranch_vccz .Lwb_1228l_1
	s_waitcnt vmcnt(8)

.Lmid_1228:
	s_add_i32 s2, 0, 0x18000
	v_add_u32_e32 v0, s2, v152
	s_add_i32 s3, 0, 0x1c000
	ds_read_b128 v[146:149], v0
	ds_read_b128 v[158:161], v0 offset:1024
	ds_read_b128 v[162:165], v0 offset:2048
	ds_read_b128 v[166:169], v0 offset:3072
	v_add_u32_e32 v0, s3, v152
	ds_read_b128 v[170:173], v0
	ds_read_b128 v[174:177], v0 offset:1024
	ds_read_b128 v[178:181], v0 offset:2048
	ds_read_b128 v[182:185], v0 offset:3072
	s_add_u32 s0, s40, 0x80000
	s_addc_u32 s1, s41, 0
	s_mov_b32 m0, s48
	v_lshl_add_u64 v[220:221], s[0:1], 0, v[130:131]
	ds_read_b128 v[186:189], v156 offset:32768
	ds_read_b128 v[190:193], v156 offset:33792
	ds_read_b128 v[194:197], v156 offset:34816
	ds_read_b128 v[198:201], v156 offset:35840
	ds_read_b128 v[202:205], v156 offset:36864
	ds_read_b128 v[206:209], v156 offset:37888
	ds_read_b128 v[210:213], v156 offset:38912
	ds_read_b128 v[214:217], v156 offset:39936
	global_load_lds_dwordx4 v[220:221], off
	v_lshl_add_u64 v[220:221], s[0:1], 0, v[134:135]
	s_mov_b32 m0, s49
	s_nop 0
	global_load_lds_dwordx4 v[220:221], off
	s_and_b64 vcc, exec, s[14:15]
	s_cbranch_vccnz .Lwa_1228l_2
	s_waitcnt vmcnt(8)

.Lwb_1228l_2:
	s_setprio 0
	s_barrier
	s_add_u32 s0, s38, 0x2000
	s_addc_u32 s1, s39, 0
	s_add_i32 s2, s2, s46
	v_lshl_add_u64 v[220:221], s[0:1], 0, v[132:133]
	s_mov_b32 m0, s2
	ds_read_b128 v[186:189], v156 offset:49152
	ds_read_b128 v[190:193], v156 offset:50176
	ds_read_b128 v[194:197], v156 offset:51200
	ds_read_b128 v[198:201], v156 offset:52224
	ds_read_b128 v[202:205], v156 offset:53248
	ds_read_b128 v[206:209], v156 offset:54272
	ds_read_b128 v[210:213], v156 offset:55296
	ds_read_b128 v[214:217], v156 offset:56320
	global_load_lds_dwordx4 v[220:221], off
	s_add_i32 m0, s2, 0x2000
	v_lshl_add_u64 v[220:221], s[0:1], 0, v[136:137]
	s_add_u32 s0, s38, 0x82000
	s_addc_u32 s1, s39, 0
	s_add_i32 s2, s3, s46
	global_load_lds_dwordx4 v[220:221], off
	v_lshl_add_u64 v[220:221], s[0:1], 0, v[132:133]
	s_mov_b32 m0, s2
	v_lshl_add_u64 v[150:151], v[150:151], 0, s[12:13]
	global_load_lds_dwordx4 v[220:221], off
	v_lshl_add_u64 v[220:221], s[0:1], 0, v[136:137]
	s_add_i32 m0, s2, 0x2000
	s_nop 0
	global_load_lds_dwordx4 v[220:221], off
	s_mov_b32 m0, s51
	s_nop 0
	global_load_lds_dwordx4 v[150:151], off
	v_lshl_add_u64 v[150:151], v[218:219], 0, s[12:13]
	s_mov_b32 m0, s52
	s_nop 0
	global_load_lds_dwordx4 v[150:151], off
	s_and_b64 vcc, exec, s[14:15]
	s_cbranch_vccnz .Lwa_1228l_3
	s_waitcnt vmcnt(8)

.Lwb_1228l_3:
	s_setprio 0
	s_barrier
	s_add_i32 s61, s61, 2
	s_add_u32 s59, s59, 0x4000
	s_addc_u32 s60, s60, 0
	s_add_u32 s36, s36, 0x100
	s_addc_u32 s37, s37, 0
	s_cmp_gt_u32 s61, 29
	s_cbranch_scc0 .LBB0_1228
	s_and_b64 vcc, exec, s[14:15]
	s_cbranch_vccz .LBB0_1231
	s_barrier

.LBB0_1481:
	s_lshl_b32 s1, s30, 7
	s_ashr_i32 s0, s30, 4
	s_and_b32 s1, s1, 0x780
	v_or_b32_e32 v240, s1, v184
	s_ashr_i32 s1, s0, 31
	s_lshl_b64 s[0:1], s[0:1], 13
	s_add_u32 s2, s8, s0
	s_addc_u32 s3, s9, s1
	v_lshlrev_b32_e32 v240, 2, v240
	s_add_u32 s0, s10, s0
	s_addc_u32 s1, s11, s1
	global_load_dwordx4 v[224:227], v240, s[2:3]
	global_load_dwordx4 v[228:231], v240, s[2:3] offset:16
	global_load_dwordx4 v[232:235], v240, s[0:1]
	global_load_dwordx4 v[236:239], v240, s[0:1] offset:16
	s_ashr_i32 s21, s20, 31
	s_lshl_b64 s[0:1], s[20:21], 19
	s_add_u32 s24, s47, s0
	s_addc_u32 s25, s48, s1
	s_and_b64 s[0:1], s[4:5], exec
	s_cselect_b32 s21, s25, s37
	s_cselect_b32 s63, s24, s36
	s_ashr_i32 s23, s22, 31
	s_lshl_b64 s[0:1], s[22:23], 19
	s_add_u32 s26, s45, s0
	s_addc_u32 s27, s46, s1
	s_and_b64 s[0:1], s[4:5], exec
	s_cselect_b32 s23, s27, s35
	s_cselect_b32 s64, s26, s34
	s_add_u32 s65, s34, 0x4000
	s_addc_u32 s66, s35, 0
	s_add_u32 s34, s36, 0x40080
	s_addc_u32 s35, s37, 0
	s_mov_b32 s67, -2
	ds_read_b128 v[26:29], v185
	ds_read_b128 v[30:33], v185 offset:1024
	ds_read_b128 v[18:21], v185 offset:2048
	ds_read_b128 v[22:25], v185 offset:3072
	ds_read_b128 v[10:13], v186
	ds_read_b128 v[14:17], v186 offset:1024
	ds_read_b128 v[2:5], v186 offset:2048
	ds_read_b128 v[6:9], v186 offset:3072
	s_add_u32 s0, s34, 0xfffc0080
	s_addc_u32 s1, s35, -1
	s_cmp_eq_u32 s67, 12
	s_cselect_b32 s39, s21, s1
	s_cselect_b32 s38, s63, s0
	s_cselect_b32 s37, s23, s66
	s_cselect_b32 s36, s64, s65
	v_lshl_add_u64 v[178:179], s[34:35], 0, v[172:173]
	s_add_i32 m0, s29, 0xc000
	ds_read_b128 v[190:193], v187
	ds_read_b128 v[194:197], v187 offset:1024
	ds_read_b128 v[198:201], v187 offset:2048
	ds_read_b128 v[202:205], v187 offset:3072
	ds_read_b128 v[206:209], v187 offset:4096
	ds_read_b128 v[210:213], v187 offset:5120
	ds_read_b128 v[214:217], v187 offset:6144
	ds_read_b128 v[218:221], v187 offset:7168
	global_load_lds_dwordx4 v[178:179], off
	v_lshl_add_u64 v[178:179], s[34:35], 0, v[174:175]
	s_add_i32 m0, s29, 0xe000
	s_nop 0
	global_load_lds_dwordx4 v[178:179], off
	s_and_b64 vcc, exec, s[18:19]
	s_cbranch_vccnz .Lwa_1482p_0
	s_waitcnt vmcnt(8)
.Lwa_1482p_0:
	s_waitcnt lgkmcnt(0)
	s_barrier
	s_setprio 1
	s_waitcnt lgkmcnt(0)
	v_mfma_scale_f32_16x16x128_f8f6f4 v[158:161], v[26:33], v[190:197], 0, v188, v188 op_sel_hi:[0,0,0]
	v_mfma_scale_f32_16x16x128_f8f6f4 v[154:157], v[18:25], v[190:197], 0, v188, v188 op_sel_hi:[0,0,0]
	v_mfma_scale_f32_16x16x128_f8f6f4 v[142:145], v[26:33], v[198:205], 0, v188, v188 op_sel_hi:[0,0,0]
	v_mfma_scale_f32_16x16x128_f8f6f4 v[138:141], v[18:25], v[198:205], 0, v188, v188 op_sel_hi:[0,0,0]
	v_mfma_scale_f32_16x16x128_f8f6f4 v[126:129], v[26:33], v[206:213], 0, v188, v188 op_sel_hi:[0,0,0]
	v_mfma_scale_f32_16x16x128_f8f6f4 v[122:125], v[18:25], v[206:213], 0, v188, v188 op_sel_hi:[0,0,0]
	v_mfma_scale_f32_16x16x128_f8f6f4 v[110:113], v[26:33], v[214:221], 0, v188, v188 op_sel_hi:[0,0,0]
	v_mfma_scale_f32_16x16x128_f8f6f4 v[106:109], v[18:25], v[214:221], 0, v188, v188 op_sel_hi:[0,0,0]
	s_setprio 0
	s_setprio 1
	v_mfma_scale_f32_16x16x128_f8f6f4 v[150:153], v[10:17], v[190:197], 0, v188, v188 op_sel_hi:[0,0,0]
	v_mfma_scale_f32_16x16x128_f8f6f4 v[146:149], v[2:9], v[190:197], 0, v188, v188 op_sel_hi:[0,0,0]
	v_mfma_scale_f32_16x16x128_f8f6f4 v[134:137], v[10:17], v[198:205], 0, v188, v188 op_sel_hi:[0,0,0]
	v_mfma_scale_f32_16x16x128_f8f6f4 v[130:133], v[2:9], v[198:205], 0, v188, v188 op_sel_hi:[0,0,0]
	v_mfma_scale_f32_16x16x128_f8f6f4 v[118:121], v[10:17], v[206:213], 0, v188, v188 op_sel_hi:[0,0,0]
	v_mfma_scale_f32_16x16x128_f8f6f4 v[114:117], v[2:9], v[206:213], 0, v188, v188 op_sel_hi:[0,0,0]
	v_mfma_scale_f32_16x16x128_f8f6f4 v[102:105], v[10:17], v[214:221], 0, v188, v188 op_sel_hi:[0,0,0]
	v_mfma_scale_f32_16x16x128_f8f6f4 v[98:101], v[2:9], v[214:221], 0, v188, v188 op_sel_hi:[0,0,0]
	s_cbranch_vccz .Lwb_1482p_0
	s_waitcnt vmcnt(8)
.Lwb_1482p_0:
	s_setprio 0
	s_barrier
	s_add_i32 s0, s57, s49
	v_lshl_add_u64 v[178:179], s[36:37], 0, v[164:165]
	s_mov_b32 m0, s0
	ds_read_b128 v[190:193], v187 offset:16384
	ds_read_b128 v[194:197], v187 offset:17408
	ds_read_b128 v[198:201], v187 offset:18432
	ds_read_b128 v[202:205], v187 offset:19456
	ds_read_b128 v[206:209], v187 offset:20480
	ds_read_b128 v[210:213], v187 offset:21504
	ds_read_b128 v[214:217], v187 offset:22528
	ds_read_b128 v[218:221], v187 offset:23552
	global_load_lds_dwordx4 v[178:179], off
	s_add_i32 m0, s0, 0x2000
	s_add_u32 s0, s36, 0x40000
	v_lshl_add_u64 v[178:179], s[36:37], 0, v[168:169]
	s_addc_u32 s1, s37, 0
	s_add_i32 s2, s58, s49
	global_load_lds_dwordx4 v[178:179], off
	v_lshl_add_u64 v[178:179], s[0:1], 0, v[164:165]
	s_mov_b32 m0, s2
	v_lshl_add_u64 v[180:181], s[38:39], 0, v[166:167]
	global_load_lds_dwordx4 v[178:179], off
	v_lshl_add_u64 v[178:179], s[0:1], 0, v[168:169]
	s_add_i32 m0, s2, 0x2000
	s_nop 0
	global_load_lds_dwordx4 v[178:179], off
	v_lshl_add_u64 v[178:179], s[38:39], 0, v[162:163]
	s_mov_b32 m0, s29
	s_nop 0
	global_load_lds_dwordx4 v[178:179], off
	s_mov_b32 m0, s31
	s_nop 0
	global_load_lds_dwordx4 v[180:181], off
	s_and_b64 vcc, exec, s[18:19]
	s_cbranch_vccnz .Lwa_1482p_1
	s_waitcnt vmcnt(8)
.Lwa_1482p_1:
	s_waitcnt lgkmcnt(0)
	s_barrier
	s_setprio 1
	s_waitcnt lgkmcnt(0)
	v_mfma_scale_f32_16x16x128_f8f6f4 v[94:97], v[26:33], v[190:197], 0, v188, v188 op_sel_hi:[0,0,0]
	v_mfma_scale_f32_16x16x128_f8f6f4 v[90:93], v[18:25], v[190:197], 0, v188, v188 op_sel_hi:[0,0,0]
	v_mfma_scale_f32_16x16x128_f8f6f4 v[78:81], v[26:33], v[198:205], 0, v188, v188 op_sel_hi:[0,0,0]
	v_mfma_scale_f32_16x16x128_f8f6f4 v[74:77], v[18:25], v[198:205], 0, v188, v188 op_sel_hi:[0,0,0]
	v_mfma_scale_f32_16x16x128_f8f6f4 v[62:65], v[26:33], v[206:213], 0, v188, v188 op_sel_hi:[0,0,0]
	v_mfma_scale_f32_16x16x128_f8f6f4 v[58:61], v[18:25], v[206:213], 0, v188, v188 op_sel_hi:[0,0,0]
	v_mfma_scale_f32_16x16x128_f8f6f4 v[46:49], v[26:33], v[214:221], 0, v188, v188 op_sel_hi:[0,0,0]
	v_mfma_scale_f32_16x16x128_f8f6f4 v[42:45], v[18:25], v[214:221], 0, v188, v188 op_sel_hi:[0,0,0]
	s_setprio 0
	s_setprio 1
	v_mfma_scale_f32_16x16x128_f8f6f4 v[86:89], v[10:17], v[190:197], 0, v188, v188 op_sel_hi:[0,0,0]
	v_mfma_scale_f32_16x16x128_f8f6f4 v[82:85], v[2:9], v[190:197], 0, v188, v188 op_sel_hi:[0,0,0]
	v_mfma_scale_f32_16x16x128_f8f6f4 v[70:73], v[10:17], v[198:205], 0, v188, v188 op_sel_hi:[0,0,0]
	v_mfma_scale_f32_16x16x128_f8f6f4 v[66:69], v[2:9], v[198:205], 0, v188, v188 op_sel_hi:[0,0,0]
	v_mfma_scale_f32_16x16x128_f8f6f4 v[54:57], v[10:17], v[206:213], 0, v188, v188 op_sel_hi:[0,0,0]
	v_mfma_scale_f32_16x16x128_f8f6f4 v[50:53], v[2:9], v[206:213], 0, v188, v188 op_sel_hi:[0,0,0]
	v_mfma_scale_f32_16x16x128_f8f6f4 v[38:41], v[10:17], v[214:221], 0, v188, v188 op_sel_hi:[0,0,0]
	v_mfma_scale_f32_16x16x128_f8f6f4 v[34:37], v[2:9], v[214:221], 0, v188, v188 op_sel_hi:[0,0,0]
	s_cbranch_vccz .Lwb_1482p_1
	s_waitcnt vmcnt(8)

.LBB0_1482:
	ds_read_b128 v[26:29], v185
	ds_read_b128 v[30:33], v185 offset:1024
	ds_read_b128 v[18:21], v185 offset:2048
	ds_read_b128 v[22:25], v185 offset:3072
	ds_read_b128 v[10:13], v186
	ds_read_b128 v[14:17], v186 offset:1024
	ds_read_b128 v[2:5], v186 offset:2048
	ds_read_b128 v[6:9], v186 offset:3072
	s_add_u32 s0, s34, 0xfffc0080
	s_addc_u32 s1, s35, -1
	s_cmp_eq_u32 s67, 12
	s_cselect_b32 s39, s21, s1
	s_cselect_b32 s38, s63, s0
	s_cselect_b32 s37, s23, s66
	s_cselect_b32 s36, s64, s65
	v_lshl_add_u64 v[178:179], s[34:35], 0, v[172:173]
	s_add_i32 m0, s29, 0xc000
	ds_read_b128 v[190:193], v187
	ds_read_b128 v[194:197], v187 offset:1024
	ds_read_b128 v[198:201], v187 offset:2048
	ds_read_b128 v[202:205], v187 offset:3072
	ds_read_b128 v[206:209], v187 offset:4096
	ds_read_b128 v[210:213], v187 offset:5120
	ds_read_b128 v[214:217], v187 offset:6144
	ds_read_b128 v[218:221], v187 offset:7168
	global_load_lds_dwordx4 v[178:179], off
	v_lshl_add_u64 v[178:179], s[34:35], 0, v[174:175]
	s_add_i32 m0, s29, 0xe000
	s_nop 0
	global_load_lds_dwordx4 v[178:179], off
	s_and_b64 vcc, exec, s[18:19]
	s_cbranch_vccnz .Lwa_1482l_0
	s_waitcnt vmcnt(8)
.Lwa_1482l_0:
	s_waitcnt lgkmcnt(0)
	s_barrier
	s_setprio 1
	s_waitcnt lgkmcnt(0)
	v_mfma_scale_f32_16x16x128_f8f6f4 v[158:161], v[26:33], v[190:197], v[158:161], v188, v188 op_sel_hi:[0,0,0]
	v_mfma_scale_f32_16x16x128_f8f6f4 v[154:157], v[18:25], v[190:197], v[154:157], v188, v188 op_sel_hi:[0,0,0]
	v_mfma_scale_f32_16x16x128_f8f6f4 v[142:145], v[26:33], v[198:205], v[142:145], v188, v188 op_sel_hi:[0,0,0]
	v_mfma_scale_f32_16x16x128_f8f6f4 v[138:141], v[18:25], v[198:205], v[138:141], v188, v188 op_sel_hi:[0,0,0]
	v_mfma_scale_f32_16x16x128_f8f6f4 v[126:129], v[26:33], v[206:213], v[126:129], v188, v188 op_sel_hi:[0,0,0]
	v_mfma_scale_f32_16x16x128_f8f6f4 v[122:125], v[18:25], v[206:213], v[122:125], v188, v188 op_sel_hi:[0,0,0]
	v_mfma_scale_f32_16x16x128_f8f6f4 v[110:113], v[26:33], v[214:221], v[110:113], v188, v188 op_sel_hi:[0,0,0]
	v_mfma_scale_f32_16x16x128_f8f6f4 v[106:109], v[18:25], v[214:221], v[106:109], v188, v188 op_sel_hi:[0,0,0]
	s_setprio 0
	s_setprio 1
	v_mfma_scale_f32_16x16x128_f8f6f4 v[150:153], v[10:17], v[190:197], v[150:153], v188, v188 op_sel_hi:[0,0,0]
	v_mfma_scale_f32_16x16x128_f8f6f4 v[146:149], v[2:9], v[190:197], v[146:149], v188, v188 op_sel_hi:[0,0,0]
	v_mfma_scale_f32_16x16x128_f8f6f4 v[134:137], v[10:17], v[198:205], v[134:137], v188, v188 op_sel_hi:[0,0,0]
	v_mfma_scale_f32_16x16x128_f8f6f4 v[130:133], v[2:9], v[198:205], v[130:133], v188, v188 op_sel_hi:[0,0,0]
	v_mfma_scale_f32_16x16x128_f8f6f4 v[118:121], v[10:17], v[206:213], v[118:121], v188, v188 op_sel_hi:[0,0,0]
	v_mfma_scale_f32_16x16x128_f8f6f4 v[114:117], v[2:9], v[206:213], v[114:117], v188, v188 op_sel_hi:[0,0,0]
	v_mfma_scale_f32_16x16x128_f8f6f4 v[102:105], v[10:17], v[214:221], v[102:105], v188, v188 op_sel_hi:[0,0,0]
	v_mfma_scale_f32_16x16x128_f8f6f4 v[98:101], v[2:9], v[214:221], v[98:101], v188, v188 op_sel_hi:[0,0,0]
	s_cbranch_vccz .Lwb_1482l_0
	s_waitcnt vmcnt(8)

.Lwa_1482l_1:
	s_waitcnt lgkmcnt(0)
	s_barrier
	s_setprio 1
	s_waitcnt lgkmcnt(0)
	v_mfma_scale_f32_16x16x128_f8f6f4 v[94:97], v[26:33], v[190:197], v[94:97], v188, v188 op_sel_hi:[0,0,0]
	v_mfma_scale_f32_16x16x128_f8f6f4 v[90:93], v[18:25], v[190:197], v[90:93], v188, v188 op_sel_hi:[0,0,0]
	v_mfma_scale_f32_16x16x128_f8f6f4 v[78:81], v[26:33], v[198:205], v[78:81], v188, v188 op_sel_hi:[0,0,0]
	v_mfma_scale_f32_16x16x128_f8f6f4 v[74:77], v[18:25], v[198:205], v[74:77], v188, v188 op_sel_hi:[0,0,0]
	v_mfma_scale_f32_16x16x128_f8f6f4 v[62:65], v[26:33], v[206:213], v[62:65], v188, v188 op_sel_hi:[0,0,0]
	v_mfma_scale_f32_16x16x128_f8f6f4 v[58:61], v[18:25], v[206:213], v[58:61], v188, v188 op_sel_hi:[0,0,0]
	v_mfma_scale_f32_16x16x128_f8f6f4 v[46:49], v[26:33], v[214:221], v[46:49], v188, v188 op_sel_hi:[0,0,0]
	v_mfma_scale_f32_16x16x128_f8f6f4 v[42:45], v[18:25], v[214:221], v[42:45], v188, v188 op_sel_hi:[0,0,0]
	s_setprio 0
	s_setprio 1
	v_mfma_scale_f32_16x16x128_f8f6f4 v[86:89], v[10:17], v[190:197], v[86:89], v188, v188 op_sel_hi:[0,0,0]
	v_mfma_scale_f32_16x16x128_f8f6f4 v[82:85], v[2:9], v[190:197], v[82:85], v188, v188 op_sel_hi:[0,0,0]
	v_mfma_scale_f32_16x16x128_f8f6f4 v[70:73], v[10:17], v[198:205], v[70:73], v188, v188 op_sel_hi:[0,0,0]
	v_mfma_scale_f32_16x16x128_f8f6f4 v[66:69], v[2:9], v[198:205], v[66:69], v188, v188 op_sel_hi:[0,0,0]
	v_mfma_scale_f32_16x16x128_f8f6f4 v[54:57], v[10:17], v[206:213], v[54:57], v188, v188 op_sel_hi:[0,0,0]
	v_mfma_scale_f32_16x16x128_f8f6f4 v[50:53], v[2:9], v[206:213], v[50:53], v188, v188 op_sel_hi:[0,0,0]
	v_mfma_scale_f32_16x16x128_f8f6f4 v[38:41], v[10:17], v[214:221], v[38:41], v188, v188 op_sel_hi:[0,0,0]
	v_mfma_scale_f32_16x16x128_f8f6f4 v[34:37], v[2:9], v[214:221], v[34:37], v188, v188 op_sel_hi:[0,0,0]
	s_cbranch_vccz .Lwb_1482l_1
	s_waitcnt vmcnt(8)

.Lmid_1482:
	s_add_i32 s2, 0, 0x18000
	v_add_u32_e32 v0, s2, v183
	s_add_i32 s3, 0, 0x1c000
	ds_read_b128 v[2:5], v0
	ds_read_b128 v[6:9], v0 offset:1024
	ds_read_b128 v[10:13], v0 offset:2048
	ds_read_b128 v[14:17], v0 offset:3072
	v_add_u32_e32 v0, s3, v183
	ds_read_b128 v[18:21], v0
	ds_read_b128 v[22:25], v0 offset:1024
	ds_read_b128 v[26:29], v0 offset:2048
	ds_read_b128 v[30:33], v0 offset:3072
	s_add_u32 s0, s38, 0x40000
	s_addc_u32 s1, s39, 0
	s_mov_b32 m0, s50
	v_lshl_add_u64 v[222:223], s[0:1], 0, v[162:163]
	ds_read_b128 v[190:193], v187 offset:32768
	ds_read_b128 v[194:197], v187 offset:33792
	ds_read_b128 v[198:201], v187 offset:34816
	ds_read_b128 v[202:205], v187 offset:35840
	ds_read_b128 v[206:209], v187 offset:36864
	ds_read_b128 v[210:213], v187 offset:37888
	ds_read_b128 v[214:217], v187 offset:38912
	ds_read_b128 v[218:221], v187 offset:39936
	global_load_lds_dwordx4 v[222:223], off
	v_lshl_add_u64 v[222:223], s[0:1], 0, v[166:167]
	s_mov_b32 m0, s51
	s_nop 0
	global_load_lds_dwordx4 v[222:223], off
	s_and_b64 vcc, exec, s[18:19]
	s_cbranch_vccnz .Lwa_1482l_2
	s_waitcnt vmcnt(8)
.Lwa_1482l_2:
	s_waitcnt lgkmcnt(0)
	s_barrier
	s_setprio 1
	s_waitcnt lgkmcnt(0)
	v_mfma_scale_f32_16x16x128_f8f6f4 v[158:161], v[2:9], v[190:197], v[158:161], v188, v188 op_sel_hi:[0,0,0]
	v_mfma_scale_f32_16x16x128_f8f6f4 v[154:157], v[10:17], v[190:197], v[154:157], v188, v188 op_sel_hi:[0,0,0]
	v_mfma_scale_f32_16x16x128_f8f6f4 v[142:145], v[2:9], v[198:205], v[142:145], v188, v188 op_sel_hi:[0,0,0]
	v_mfma_scale_f32_16x16x128_f8f6f4 v[138:141], v[10:17], v[198:205], v[138:141], v188, v188 op_sel_hi:[0,0,0]
	v_mfma_scale_f32_16x16x128_f8f6f4 v[126:129], v[2:9], v[206:213], v[126:129], v188, v188 op_sel_hi:[0,0,0]
	v_mfma_scale_f32_16x16x128_f8f6f4 v[122:125], v[10:17], v[206:213], v[122:125], v188, v188 op_sel_hi:[0,0,0]
	v_mfma_scale_f32_16x16x128_f8f6f4 v[110:113], v[2:9], v[214:221], v[110:113], v188, v188 op_sel_hi:[0,0,0]
	v_mfma_scale_f32_16x16x128_f8f6f4 v[106:109], v[10:17], v[214:221], v[106:109], v188, v188 op_sel_hi:[0,0,0]
	s_setprio 0
	s_setprio 1
	v_mfma_scale_f32_16x16x128_f8f6f4 v[150:153], v[18:25], v[190:197], v[150:153], v188, v188 op_sel_hi:[0,0,0]
	v_mfma_scale_f32_16x16x128_f8f6f4 v[146:149], v[26:33], v[190:197], v[146:149], v188, v188 op_sel_hi:[0,0,0]
	v_mfma_scale_f32_16x16x128_f8f6f4 v[134:137], v[18:25], v[198:205], v[134:137], v188, v188 op_sel_hi:[0,0,0]
	v_mfma_scale_f32_16x16x128_f8f6f4 v[130:133], v[26:33], v[198:205], v[130:133], v188, v188 op_sel_hi:[0,0,0]
	v_mfma_scale_f32_16x16x128_f8f6f4 v[118:121], v[18:25], v[206:213], v[118:121], v188, v188 op_sel_hi:[0,0,0]
	v_mfma_scale_f32_16x16x128_f8f6f4 v[114:117], v[26:33], v[206:213], v[114:117], v188, v188 op_sel_hi:[0,0,0]
	v_mfma_scale_f32_16x16x128_f8f6f4 v[102:105], v[18:25], v[214:221], v[102:105], v188, v188 op_sel_hi:[0,0,0]
	v_mfma_scale_f32_16x16x128_f8f6f4 v[98:101], v[26:33], v[214:221], v[98:101], v188, v188 op_sel_hi:[0,0,0]
	s_cbranch_vccz .Lwb_1482l_2
	s_waitcnt vmcnt(8)
.Lwb_1482l_2:
	s_setprio 0
	s_barrier
	s_add_u32 s0, s36, 0x2000
	s_addc_u32 s1, s37, 0
	s_add_i32 s2, s2, s49
	v_lshl_add_u64 v[222:223], s[0:1], 0, v[164:165]
	s_mov_b32 m0, s2
	ds_read_b128 v[190:193], v187 offset:49152
	ds_read_b128 v[194:197], v187 offset:50176
	ds_read_b128 v[198:201], v187 offset:51200
	ds_read_b128 v[202:205], v187 offset:52224
	ds_read_b128 v[206:209], v187 offset:53248
	ds_read_b128 v[210:213], v187 offset:54272
	ds_read_b128 v[214:217], v187 offset:55296
	ds_read_b128 v[218:221], v187 offset:56320
	global_load_lds_dwordx4 v[222:223], off
	s_add_i32 m0, s2, 0x2000
	v_lshl_add_u64 v[222:223], s[0:1], 0, v[168:169]
	s_add_u32 s0, s36, 0x42000
	s_addc_u32 s1, s37, 0
	s_add_i32 s2, s3, s49
	global_load_lds_dwordx4 v[222:223], off
	v_lshl_add_u64 v[222:223], s[0:1], 0, v[164:165]
	s_mov_b32 m0, s2
	v_lshl_add_u64 v[178:179], v[178:179], 0, s[16:17]
	global_load_lds_dwordx4 v[222:223], off
	v_lshl_add_u64 v[222:223], s[0:1], 0, v[168:169]
	s_add_i32 m0, s2, 0x2000
	s_nop 0
	global_load_lds_dwordx4 v[222:223], off
	s_mov_b32 m0, s53
	s_nop 0
	global_load_lds_dwordx4 v[178:179], off
	v_lshl_add_u64 v[178:179], v[180:181], 0, s[16:17]
	s_mov_b32 m0, s54
	s_nop 0
	global_load_lds_dwordx4 v[178:179], off
	s_and_b64 vcc, exec, s[18:19]
	s_cbranch_vccnz .Lwa_1482l_3
	s_waitcnt vmcnt(8)
.Lwa_1482l_3:
	s_waitcnt lgkmcnt(0)
	s_barrier
	s_setprio 1
	s_waitcnt lgkmcnt(0)
	v_mfma_scale_f32_16x16x128_f8f6f4 v[94:97], v[2:9], v[190:197], v[94:97], v188, v188 op_sel_hi:[0,0,0]
	v_mfma_scale_f32_16x16x128_f8f6f4 v[90:93], v[10:17], v[190:197], v[90:93], v188, v188 op_sel_hi:[0,0,0]
	v_mfma_scale_f32_16x16x128_f8f6f4 v[78:81], v[2:9], v[198:205], v[78:81], v188, v188 op_sel_hi:[0,0,0]
	v_mfma_scale_f32_16x16x128_f8f6f4 v[74:77], v[10:17], v[198:205], v[74:77], v188, v188 op_sel_hi:[0,0,0]
	v_mfma_scale_f32_16x16x128_f8f6f4 v[62:65], v[2:9], v[206:213], v[62:65], v188, v188 op_sel_hi:[0,0,0]
	v_mfma_scale_f32_16x16x128_f8f6f4 v[58:61], v[10:17], v[206:213], v[58:61], v188, v188 op_sel_hi:[0,0,0]
	v_mfma_scale_f32_16x16x128_f8f6f4 v[46:49], v[2:9], v[214:221], v[46:49], v188, v188 op_sel_hi:[0,0,0]
	v_mfma_scale_f32_16x16x128_f8f6f4 v[42:45], v[10:17], v[214:221], v[42:45], v188, v188 op_sel_hi:[0,0,0]
	s_setprio 0
	s_setprio 1
	v_mfma_scale_f32_16x16x128_f8f6f4 v[86:89], v[18:25], v[190:197], v[86:89], v188, v188 op_sel_hi:[0,0,0]
	v_mfma_scale_f32_16x16x128_f8f6f4 v[82:85], v[26:33], v[190:197], v[82:85], v188, v188 op_sel_hi:[0,0,0]
	v_mfma_scale_f32_16x16x128_f8f6f4 v[70:73], v[18:25], v[198:205], v[70:73], v188, v188 op_sel_hi:[0,0,0]
	v_mfma_scale_f32_16x16x128_f8f6f4 v[66:69], v[26:33], v[198:205], v[66:69], v188, v188 op_sel_hi:[0,0,0]
	v_mfma_scale_f32_16x16x128_f8f6f4 v[54:57], v[18:25], v[206:213], v[54:57], v188, v188 op_sel_hi:[0,0,0]
	v_mfma_scale_f32_16x16x128_f8f6f4 v[50:53], v[26:33], v[206:213], v[50:53], v188, v188 op_sel_hi:[0,0,0]
	v_mfma_scale_f32_16x16x128_f8f6f4 v[38:41], v[18:25], v[214:221], v[38:41], v188, v188 op_sel_hi:[0,0,0]
	v_mfma_scale_f32_16x16x128_f8f6f4 v[34:37], v[26:33], v[214:221], v[34:37], v188, v188 op_sel_hi:[0,0,0]
	s_cbranch_vccz .Lwb_1482l_3
	s_waitcnt vmcnt(8)
.Lwb_1482l_3:
	s_setprio 0
	s_barrier
	s_add_i32 s67, s67, 2
	s_add_u32 s65, s65, 0x4000
	s_addc_u32 s66, s66, 0
	s_add_u32 s34, s34, 0x100
	s_addc_u32 s35, s35, 0
	s_cmp_gt_u32 s67, 13
	s_cbranch_scc0 .LBB0_1482
	s_and_b64 vcc, exec, s[18:19]
	s_cbranch_vccz .LBB0_1485
	s_barrier

.LBB0_1576:
	s_lshl_b32 s1, s38, 8
	s_ashr_i32 s0, s38, 3
	s_and_b32 s1, s1, 0x700
	v_or_b32_e32 v240, s1, v183
	s_ashr_i32 s1, s0, 31
	s_lshl_b64 s[0:1], s[0:1], 13
	s_add_u32 s2, s6, s0
	s_addc_u32 s3, s7, s1
	v_lshlrev_b32_e32 v240, 2, v240
	global_load_dwordx4 v[224:227], v240, s[2:3]
	global_load_dwordx4 v[228:231], v240, s[2:3] offset:16
	global_load_dwordx4 v[232:235], v240, s[2:3] offset:512
	global_load_dwordx4 v[236:239], v240, s[2:3] offset:528
	s_ashr_i32 s27, s26, 31
	s_lshl_b64 s[0:1], s[26:27], 19
	s_add_u32 s30, s49, s0
	s_addc_u32 s31, s50, s1
	s_and_b64 s[0:1], s[4:5], exec
	s_cselect_b32 s27, s31, s43
	s_cselect_b32 s39, s30, s42
	s_ashr_i32 s29, s28, 31
	s_lshl_b64 s[0:1], s[28:29], 19
	s_add_u32 s34, s51, s0
	s_addc_u32 s35, s52, s1
	s_and_b64 s[0:1], s[4:5], exec
	s_cselect_b32 s29, s35, s41
	s_cselect_b32 s68, s34, s40
	s_add_u32 s69, s40, 0x4000
	s_addc_u32 s70, s41, 0
	s_add_u32 s40, s42, 0x40080
	s_addc_u32 s41, s43, 0
	s_mov_b32 s71, -2
	ds_read_b128 v[26:29], v184
	ds_read_b128 v[30:33], v184 offset:1024
	ds_read_b128 v[18:21], v184 offset:2048
	ds_read_b128 v[22:25], v184 offset:3072
	ds_read_b128 v[10:13], v185
	ds_read_b128 v[14:17], v185 offset:1024
	ds_read_b128 v[2:5], v185 offset:2048
	ds_read_b128 v[6:9], v185 offset:3072
	s_add_u32 s0, s40, 0xfffc0080
	s_addc_u32 s1, s41, -1
	s_cmp_eq_u32 s71, 12
	s_cselect_b32 s45, s27, s1
	s_cselect_b32 s44, s39, s0
	s_cselect_b32 s43, s29, s70
	s_cselect_b32 s42, s68, s69
	v_lshl_add_u64 v[178:179], s[40:41], 0, v[172:173]
	s_add_i32 m0, s37, 0xc000
	ds_read_b128 v[188:191], v186
	ds_read_b128 v[192:195], v186 offset:1024
	ds_read_b128 v[196:199], v186 offset:2048
	ds_read_b128 v[200:203], v186 offset:3072
	ds_read_b128 v[204:207], v186 offset:4096
	ds_read_b128 v[208:211], v186 offset:5120
	ds_read_b128 v[212:215], v186 offset:6144
	ds_read_b128 v[216:219], v186 offset:7168
	global_load_lds_dwordx4 v[178:179], off
	v_lshl_add_u64 v[178:179], s[40:41], 0, v[174:175]
	s_add_i32 m0, s37, 0xe000
	s_nop 0
	global_load_lds_dwordx4 v[178:179], off
	s_and_b64 vcc, exec, s[16:17]
	s_cbranch_vccnz .Lwa_1577p_0
	s_waitcnt vmcnt(8)
.Lwa_1577p_0:
	s_waitcnt lgkmcnt(0)
	s_barrier
	s_setprio 1
	s_waitcnt lgkmcnt(0)
	v_mfma_scale_f32_16x16x128_f8f6f4 v[158:161], v[26:33], v[188:195], 0, v187, v187 op_sel_hi:[0,0,0]
	v_mfma_scale_f32_16x16x128_f8f6f4 v[154:157], v[18:25], v[188:195], 0, v187, v187 op_sel_hi:[0,0,0]
	v_mfma_scale_f32_16x16x128_f8f6f4 v[150:153], v[26:33], v[196:203], 0, v187, v187 op_sel_hi:[0,0,0]
	v_mfma_scale_f32_16x16x128_f8f6f4 v[146:149], v[18:25], v[196:203], 0, v187, v187 op_sel_hi:[0,0,0]
	v_mfma_scale_f32_16x16x128_f8f6f4 v[142:145], v[26:33], v[204:211], 0, v187, v187 op_sel_hi:[0,0,0]
	v_mfma_scale_f32_16x16x128_f8f6f4 v[138:141], v[18:25], v[204:211], 0, v187, v187 op_sel_hi:[0,0,0]
	v_mfma_scale_f32_16x16x128_f8f6f4 v[134:137], v[26:33], v[212:219], 0, v187, v187 op_sel_hi:[0,0,0]
	v_mfma_scale_f32_16x16x128_f8f6f4 v[130:133], v[18:25], v[212:219], 0, v187, v187 op_sel_hi:[0,0,0]
	s_setprio 0
	s_setprio 1
	v_mfma_scale_f32_16x16x128_f8f6f4 v[102:105], v[10:17], v[188:195], 0, v187, v187 op_sel_hi:[0,0,0]
	v_mfma_scale_f32_16x16x128_f8f6f4 v[98:101], v[2:9], v[188:195], 0, v187, v187 op_sel_hi:[0,0,0]
	v_mfma_scale_f32_16x16x128_f8f6f4 v[86:89], v[10:17], v[196:203], 0, v187, v187 op_sel_hi:[0,0,0]
	v_mfma_scale_f32_16x16x128_f8f6f4 v[82:85], v[2:9], v[196:203], 0, v187, v187 op_sel_hi:[0,0,0]
	v_mfma_scale_f32_16x16x128_f8f6f4 v[78:81], v[10:17], v[204:211], 0, v187, v187 op_sel_hi:[0,0,0]
	v_mfma_scale_f32_16x16x128_f8f6f4 v[74:77], v[2:9], v[204:211], 0, v187, v187 op_sel_hi:[0,0,0]
	v_mfma_scale_f32_16x16x128_f8f6f4 v[70:73], v[10:17], v[212:219], 0, v187, v187 op_sel_hi:[0,0,0]
	v_mfma_scale_f32_16x16x128_f8f6f4 v[66:69], v[2:9], v[212:219], 0, v187, v187 op_sel_hi:[0,0,0]
	s_cbranch_vccz .Lwb_1577p_0
	s_waitcnt vmcnt(8)
.Lwb_1577p_0:
	s_setprio 0
	s_barrier
	s_add_i32 s0, s62, s53
	v_lshl_add_u64 v[178:179], s[42:43], 0, v[164:165]
	s_mov_b32 m0, s0
	ds_read_b128 v[188:191], v186 offset:16384
	ds_read_b128 v[192:195], v186 offset:17408
	ds_read_b128 v[196:199], v186 offset:18432
	ds_read_b128 v[200:203], v186 offset:19456
	ds_read_b128 v[204:207], v186 offset:20480
	ds_read_b128 v[208:211], v186 offset:21504
	ds_read_b128 v[212:215], v186 offset:22528
	ds_read_b128 v[216:219], v186 offset:23552
	global_load_lds_dwordx4 v[178:179], off
	s_add_i32 m0, s0, 0x2000
	s_add_u32 s0, s42, 0x40000
	v_lshl_add_u64 v[178:179], s[42:43], 0, v[168:169]
	s_addc_u32 s1, s43, 0
	s_add_i32 s2, s63, s53
	global_load_lds_dwordx4 v[178:179], off
	v_lshl_add_u64 v[178:179], s[0:1], 0, v[164:165]
	s_mov_b32 m0, s2
	v_lshl_add_u64 v[180:181], s[44:45], 0, v[166:167]
	global_load_lds_dwordx4 v[178:179], off
	v_lshl_add_u64 v[178:179], s[0:1], 0, v[168:169]
	s_add_i32 m0, s2, 0x2000
	s_nop 0
	global_load_lds_dwordx4 v[178:179], off
	v_lshl_add_u64 v[178:179], s[44:45], 0, v[162:163]
	s_mov_b32 m0, s37
	s_nop 0
	global_load_lds_dwordx4 v[178:179], off
	s_mov_b32 m0, s54
	s_nop 0
	global_load_lds_dwordx4 v[180:181], off
	s_and_b64 vcc, exec, s[16:17]
	s_cbranch_vccnz .Lwa_1577p_1
	s_waitcnt vmcnt(8)
.Lwa_1577p_1:
	s_waitcnt lgkmcnt(0)
	s_barrier
	s_setprio 1
	s_waitcnt lgkmcnt(0)
	v_mfma_scale_f32_16x16x128_f8f6f4 v[126:129], v[26:33], v[188:195], 0, v187, v187 op_sel_hi:[0,0,0]
	v_mfma_scale_f32_16x16x128_f8f6f4 v[122:125], v[18:25], v[188:195], 0, v187, v187 op_sel_hi:[0,0,0]
	v_mfma_scale_f32_16x16x128_f8f6f4 v[118:121], v[26:33], v[196:203], 0, v187, v187 op_sel_hi:[0,0,0]
	v_mfma_scale_f32_16x16x128_f8f6f4 v[114:117], v[18:25], v[196:203], 0, v187, v187 op_sel_hi:[0,0,0]
	v_mfma_scale_f32_16x16x128_f8f6f4 v[110:113], v[26:33], v[204:211], 0, v187, v187 op_sel_hi:[0,0,0]
	v_mfma_scale_f32_16x16x128_f8f6f4 v[106:109], v[18:25], v[204:211], 0, v187, v187 op_sel_hi:[0,0,0]
	v_mfma_scale_f32_16x16x128_f8f6f4 v[94:97], v[26:33], v[212:219], 0, v187, v187 op_sel_hi:[0,0,0]
	v_mfma_scale_f32_16x16x128_f8f6f4 v[90:93], v[18:25], v[212:219], 0, v187, v187 op_sel_hi:[0,0,0]
	s_setprio 0
	s_setprio 1
	v_mfma_scale_f32_16x16x128_f8f6f4 v[62:65], v[10:17], v[188:195], 0, v187, v187 op_sel_hi:[0,0,0]
	v_mfma_scale_f32_16x16x128_f8f6f4 v[58:61], v[2:9], v[188:195], 0, v187, v187 op_sel_hi:[0,0,0]
	v_mfma_scale_f32_16x16x128_f8f6f4 v[54:57], v[10:17], v[196:203], 0, v187, v187 op_sel_hi:[0,0,0]
	v_mfma_scale_f32_16x16x128_f8f6f4 v[50:53], v[2:9], v[196:203], 0, v187, v187 op_sel_hi:[0,0,0]
	v_mfma_scale_f32_16x16x128_f8f6f4 v[46:49], v[10:17], v[204:211], 0, v187, v187 op_sel_hi:[0,0,0]
	v_mfma_scale_f32_16x16x128_f8f6f4 v[42:45], v[2:9], v[204:211], 0, v187, v187 op_sel_hi:[0,0,0]
	v_mfma_scale_f32_16x16x128_f8f6f4 v[38:41], v[10:17], v[212:219], 0, v187, v187 op_sel_hi:[0,0,0]
	v_mfma_scale_f32_16x16x128_f8f6f4 v[34:37], v[2:9], v[212:219], 0, v187, v187 op_sel_hi:[0,0,0]
	s_cbranch_vccz .Lwb_1577p_1
	s_waitcnt vmcnt(8)

.LBB0_1577:
	ds_read_b128 v[26:29], v184
	ds_read_b128 v[30:33], v184 offset:1024
	ds_read_b128 v[18:21], v184 offset:2048
	ds_read_b128 v[22:25], v184 offset:3072
	ds_read_b128 v[10:13], v185
	ds_read_b128 v[14:17], v185 offset:1024
	ds_read_b128 v[2:5], v185 offset:2048
	ds_read_b128 v[6:9], v185 offset:3072
	s_add_u32 s0, s40, 0xfffc0080
	s_addc_u32 s1, s41, -1
	s_cmp_eq_u32 s71, 12
	s_cselect_b32 s45, s27, s1
	s_cselect_b32 s44, s39, s0
	s_cselect_b32 s43, s29, s70
	s_cselect_b32 s42, s68, s69
	v_lshl_add_u64 v[178:179], s[40:41], 0, v[172:173]
	s_add_i32 m0, s37, 0xc000
	ds_read_b128 v[188:191], v186
	ds_read_b128 v[192:195], v186 offset:1024
	ds_read_b128 v[196:199], v186 offset:2048
	ds_read_b128 v[200:203], v186 offset:3072
	ds_read_b128 v[204:207], v186 offset:4096
	ds_read_b128 v[208:211], v186 offset:5120
	ds_read_b128 v[212:215], v186 offset:6144
	ds_read_b128 v[216:219], v186 offset:7168
	global_load_lds_dwordx4 v[178:179], off
	v_lshl_add_u64 v[178:179], s[40:41], 0, v[174:175]
	s_add_i32 m0, s37, 0xe000
	s_nop 0
	global_load_lds_dwordx4 v[178:179], off
	s_and_b64 vcc, exec, s[16:17]
	s_cbranch_vccnz .Lwa_1577l_0
	s_waitcnt vmcnt(8)
.Lwa_1577l_0:
	s_waitcnt lgkmcnt(0)
	s_barrier
	s_setprio 1
	s_waitcnt lgkmcnt(0)
	v_mfma_scale_f32_16x16x128_f8f6f4 v[158:161], v[26:33], v[188:195], v[158:161], v187, v187 op_sel_hi:[0,0,0]
	v_mfma_scale_f32_16x16x128_f8f6f4 v[154:157], v[18:25], v[188:195], v[154:157], v187, v187 op_sel_hi:[0,0,0]
	v_mfma_scale_f32_16x16x128_f8f6f4 v[150:153], v[26:33], v[196:203], v[150:153], v187, v187 op_sel_hi:[0,0,0]
	v_mfma_scale_f32_16x16x128_f8f6f4 v[146:149], v[18:25], v[196:203], v[146:149], v187, v187 op_sel_hi:[0,0,0]
	v_mfma_scale_f32_16x16x128_f8f6f4 v[142:145], v[26:33], v[204:211], v[142:145], v187, v187 op_sel_hi:[0,0,0]
	v_mfma_scale_f32_16x16x128_f8f6f4 v[138:141], v[18:25], v[204:211], v[138:141], v187, v187 op_sel_hi:[0,0,0]
	v_mfma_scale_f32_16x16x128_f8f6f4 v[134:137], v[26:33], v[212:219], v[134:137], v187, v187 op_sel_hi:[0,0,0]
	v_mfma_scale_f32_16x16x128_f8f6f4 v[130:133], v[18:25], v[212:219], v[130:133], v187, v187 op_sel_hi:[0,0,0]
	s_setprio 0
	s_setprio 1
	v_mfma_scale_f32_16x16x128_f8f6f4 v[102:105], v[10:17], v[188:195], v[102:105], v187, v187 op_sel_hi:[0,0,0]
	v_mfma_scale_f32_16x16x128_f8f6f4 v[98:101], v[2:9], v[188:195], v[98:101], v187, v187 op_sel_hi:[0,0,0]
	v_mfma_scale_f32_16x16x128_f8f6f4 v[86:89], v[10:17], v[196:203], v[86:89], v187, v187 op_sel_hi:[0,0,0]
	v_mfma_scale_f32_16x16x128_f8f6f4 v[82:85], v[2:9], v[196:203], v[82:85], v187, v187 op_sel_hi:[0,0,0]
	v_mfma_scale_f32_16x16x128_f8f6f4 v[78:81], v[10:17], v[204:211], v[78:81], v187, v187 op_sel_hi:[0,0,0]
	v_mfma_scale_f32_16x16x128_f8f6f4 v[74:77], v[2:9], v[204:211], v[74:77], v187, v187 op_sel_hi:[0,0,0]
	v_mfma_scale_f32_16x16x128_f8f6f4 v[70:73], v[10:17], v[212:219], v[70:73], v187, v187 op_sel_hi:[0,0,0]
	v_mfma_scale_f32_16x16x128_f8f6f4 v[66:69], v[2:9], v[212:219], v[66:69], v187, v187 op_sel_hi:[0,0,0]
	s_cbranch_vccz .Lwb_1577l_0
	s_waitcnt vmcnt(8)

.Lwa_1577l_1:
	s_waitcnt lgkmcnt(0)
	s_barrier
	s_setprio 1
	s_waitcnt lgkmcnt(0)
	v_mfma_scale_f32_16x16x128_f8f6f4 v[126:129], v[26:33], v[188:195], v[126:129], v187, v187 op_sel_hi:[0,0,0]
	v_mfma_scale_f32_16x16x128_f8f6f4 v[122:125], v[18:25], v[188:195], v[122:125], v187, v187 op_sel_hi:[0,0,0]
	v_mfma_scale_f32_16x16x128_f8f6f4 v[118:121], v[26:33], v[196:203], v[118:121], v187, v187 op_sel_hi:[0,0,0]
	v_mfma_scale_f32_16x16x128_f8f6f4 v[114:117], v[18:25], v[196:203], v[114:117], v187, v187 op_sel_hi:[0,0,0]
	v_mfma_scale_f32_16x16x128_f8f6f4 v[110:113], v[26:33], v[204:211], v[110:113], v187, v187 op_sel_hi:[0,0,0]
	v_mfma_scale_f32_16x16x128_f8f6f4 v[106:109], v[18:25], v[204:211], v[106:109], v187, v187 op_sel_hi:[0,0,0]
	v_mfma_scale_f32_16x16x128_f8f6f4 v[94:97], v[26:33], v[212:219], v[94:97], v187, v187 op_sel_hi:[0,0,0]
	v_mfma_scale_f32_16x16x128_f8f6f4 v[90:93], v[18:25], v[212:219], v[90:93], v187, v187 op_sel_hi:[0,0,0]
	s_setprio 0
	s_setprio 1
	v_mfma_scale_f32_16x16x128_f8f6f4 v[62:65], v[10:17], v[188:195], v[62:65], v187, v187 op_sel_hi:[0,0,0]
	v_mfma_scale_f32_16x16x128_f8f6f4 v[58:61], v[2:9], v[188:195], v[58:61], v187, v187 op_sel_hi:[0,0,0]
	v_mfma_scale_f32_16x16x128_f8f6f4 v[54:57], v[10:17], v[196:203], v[54:57], v187, v187 op_sel_hi:[0,0,0]
	v_mfma_scale_f32_16x16x128_f8f6f4 v[50:53], v[2:9], v[196:203], v[50:53], v187, v187 op_sel_hi:[0,0,0]
	v_mfma_scale_f32_16x16x128_f8f6f4 v[46:49], v[10:17], v[204:211], v[46:49], v187, v187 op_sel_hi:[0,0,0]
	v_mfma_scale_f32_16x16x128_f8f6f4 v[42:45], v[2:9], v[204:211], v[42:45], v187, v187 op_sel_hi:[0,0,0]
	v_mfma_scale_f32_16x16x128_f8f6f4 v[38:41], v[10:17], v[212:219], v[38:41], v187, v187 op_sel_hi:[0,0,0]
	v_mfma_scale_f32_16x16x128_f8f6f4 v[34:37], v[2:9], v[212:219], v[34:37], v187, v187 op_sel_hi:[0,0,0]
	s_cbranch_vccz .Lwb_1577l_1
	s_waitcnt vmcnt(8)

.Lmid_1577:
	s_add_i32 s2, 0, 0x18000
	v_add_u32_e32 v0, s2, v182
	s_add_i32 s3, 0, 0x1c000
	ds_read_b128 v[2:5], v0
	ds_read_b128 v[6:9], v0 offset:1024
	ds_read_b128 v[10:13], v0 offset:2048
	ds_read_b128 v[14:17], v0 offset:3072
	v_add_u32_e32 v0, s3, v182
	ds_read_b128 v[18:21], v0
	ds_read_b128 v[22:25], v0 offset:1024
	ds_read_b128 v[26:29], v0 offset:2048
	ds_read_b128 v[30:33], v0 offset:3072
	s_add_u32 s0, s44, 0x40000
	s_addc_u32 s1, s45, 0
	s_mov_b32 m0, s55
	v_lshl_add_u64 v[220:221], s[0:1], 0, v[162:163]
	ds_read_b128 v[188:191], v186 offset:32768
	ds_read_b128 v[192:195], v186 offset:33792
	ds_read_b128 v[196:199], v186 offset:34816
	ds_read_b128 v[200:203], v186 offset:35840
	ds_read_b128 v[204:207], v186 offset:36864
	ds_read_b128 v[208:211], v186 offset:37888
	ds_read_b128 v[212:215], v186 offset:38912
	ds_read_b128 v[216:219], v186 offset:39936
	global_load_lds_dwordx4 v[220:221], off
	v_lshl_add_u64 v[220:221], s[0:1], 0, v[166:167]
	s_mov_b32 m0, s56
	s_nop 0
	global_load_lds_dwordx4 v[220:221], off
	s_and_b64 vcc, exec, s[16:17]
	s_cbranch_vccnz .Lwa_1577l_2
	s_waitcnt vmcnt(8)
.Lwa_1577l_2:
	s_waitcnt lgkmcnt(0)
	s_barrier
	s_setprio 1
	s_waitcnt lgkmcnt(0)
	v_mfma_scale_f32_16x16x128_f8f6f4 v[158:161], v[2:9], v[188:195], v[158:161], v187, v187 op_sel_hi:[0,0,0]
	v_mfma_scale_f32_16x16x128_f8f6f4 v[154:157], v[10:17], v[188:195], v[154:157], v187, v187 op_sel_hi:[0,0,0]
	v_mfma_scale_f32_16x16x128_f8f6f4 v[150:153], v[2:9], v[196:203], v[150:153], v187, v187 op_sel_hi:[0,0,0]
	v_mfma_scale_f32_16x16x128_f8f6f4 v[146:149], v[10:17], v[196:203], v[146:149], v187, v187 op_sel_hi:[0,0,0]
	v_mfma_scale_f32_16x16x128_f8f6f4 v[142:145], v[2:9], v[204:211], v[142:145], v187, v187 op_sel_hi:[0,0,0]
	v_mfma_scale_f32_16x16x128_f8f6f4 v[138:141], v[10:17], v[204:211], v[138:141], v187, v187 op_sel_hi:[0,0,0]
	v_mfma_scale_f32_16x16x128_f8f6f4 v[134:137], v[2:9], v[212:219], v[134:137], v187, v187 op_sel_hi:[0,0,0]
	v_mfma_scale_f32_16x16x128_f8f6f4 v[130:133], v[10:17], v[212:219], v[130:133], v187, v187 op_sel_hi:[0,0,0]
	s_setprio 0
	s_setprio 1
	v_mfma_scale_f32_16x16x128_f8f6f4 v[102:105], v[18:25], v[188:195], v[102:105], v187, v187 op_sel_hi:[0,0,0]
	v_mfma_scale_f32_16x16x128_f8f6f4 v[98:101], v[26:33], v[188:195], v[98:101], v187, v187 op_sel_hi:[0,0,0]
	v_mfma_scale_f32_16x16x128_f8f6f4 v[86:89], v[18:25], v[196:203], v[86:89], v187, v187 op_sel_hi:[0,0,0]
	v_mfma_scale_f32_16x16x128_f8f6f4 v[82:85], v[26:33], v[196:203], v[82:85], v187, v187 op_sel_hi:[0,0,0]
	v_mfma_scale_f32_16x16x128_f8f6f4 v[78:81], v[18:25], v[204:211], v[78:81], v187, v187 op_sel_hi:[0,0,0]
	v_mfma_scale_f32_16x16x128_f8f6f4 v[74:77], v[26:33], v[204:211], v[74:77], v187, v187 op_sel_hi:[0,0,0]
	v_mfma_scale_f32_16x16x128_f8f6f4 v[70:73], v[18:25], v[212:219], v[70:73], v187, v187 op_sel_hi:[0,0,0]
	v_mfma_scale_f32_16x16x128_f8f6f4 v[66:69], v[26:33], v[212:219], v[66:69], v187, v187 op_sel_hi:[0,0,0]
	s_cbranch_vccz .Lwb_1577l_2
	s_waitcnt vmcnt(8)
.Lwb_1577l_2:
	s_setprio 0
	s_barrier
	s_add_u32 s0, s42, 0x2000
	s_addc_u32 s1, s43, 0
	s_add_i32 s2, s2, s53
	v_lshl_add_u64 v[220:221], s[0:1], 0, v[164:165]
	s_mov_b32 m0, s2
	ds_read_b128 v[188:191], v186 offset:49152
	ds_read_b128 v[192:195], v186 offset:50176
	ds_read_b128 v[196:199], v186 offset:51200
	ds_read_b128 v[200:203], v186 offset:52224
	ds_read_b128 v[204:207], v186 offset:53248
	ds_read_b128 v[208:211], v186 offset:54272
	ds_read_b128 v[212:215], v186 offset:55296
	ds_read_b128 v[216:219], v186 offset:56320
	global_load_lds_dwordx4 v[220:221], off
	s_add_i32 m0, s2, 0x2000
	v_lshl_add_u64 v[220:221], s[0:1], 0, v[168:169]
	s_add_u32 s0, s42, 0x42000
	s_addc_u32 s1, s43, 0
	s_add_i32 s2, s3, s53
	global_load_lds_dwordx4 v[220:221], off
	v_lshl_add_u64 v[220:221], s[0:1], 0, v[164:165]
	s_mov_b32 m0, s2
	v_lshl_add_u64 v[178:179], v[178:179], 0, s[14:15]
	global_load_lds_dwordx4 v[220:221], off
	v_lshl_add_u64 v[220:221], s[0:1], 0, v[168:169]
	s_add_i32 m0, s2, 0x2000
	s_nop 0
	global_load_lds_dwordx4 v[220:221], off
	s_mov_b32 m0, s58
	s_nop 0
	global_load_lds_dwordx4 v[178:179], off
	v_lshl_add_u64 v[178:179], v[180:181], 0, s[14:15]
	s_mov_b32 m0, s59
	s_nop 0
	global_load_lds_dwordx4 v[178:179], off
	s_and_b64 vcc, exec, s[16:17]
	s_cbranch_vccnz .Lwa_1577l_3
	s_waitcnt vmcnt(8)
.Lwa_1577l_3:
	s_waitcnt lgkmcnt(0)
	s_barrier
	s_setprio 1
	s_waitcnt lgkmcnt(0)
	v_mfma_scale_f32_16x16x128_f8f6f4 v[126:129], v[2:9], v[188:195], v[126:129], v187, v187 op_sel_hi:[0,0,0]
	v_mfma_scale_f32_16x16x128_f8f6f4 v[122:125], v[10:17], v[188:195], v[122:125], v187, v187 op_sel_hi:[0,0,0]
	v_mfma_scale_f32_16x16x128_f8f6f4 v[118:121], v[2:9], v[196:203], v[118:121], v187, v187 op_sel_hi:[0,0,0]
	v_mfma_scale_f32_16x16x128_f8f6f4 v[114:117], v[10:17], v[196:203], v[114:117], v187, v187 op_sel_hi:[0,0,0]
	v_mfma_scale_f32_16x16x128_f8f6f4 v[110:113], v[2:9], v[204:211], v[110:113], v187, v187 op_sel_hi:[0,0,0]
	v_mfma_scale_f32_16x16x128_f8f6f4 v[106:109], v[10:17], v[204:211], v[106:109], v187, v187 op_sel_hi:[0,0,0]
	v_mfma_scale_f32_16x16x128_f8f6f4 v[94:97], v[2:9], v[212:219], v[94:97], v187, v187 op_sel_hi:[0,0,0]
	v_mfma_scale_f32_16x16x128_f8f6f4 v[90:93], v[10:17], v[212:219], v[90:93], v187, v187 op_sel_hi:[0,0,0]
	s_setprio 0
	s_setprio 1
	v_mfma_scale_f32_16x16x128_f8f6f4 v[62:65], v[18:25], v[188:195], v[62:65], v187, v187 op_sel_hi:[0,0,0]
	v_mfma_scale_f32_16x16x128_f8f6f4 v[58:61], v[26:33], v[188:195], v[58:61], v187, v187 op_sel_hi:[0,0,0]
	v_mfma_scale_f32_16x16x128_f8f6f4 v[54:57], v[18:25], v[196:203], v[54:57], v187, v187 op_sel_hi:[0,0,0]
	v_mfma_scale_f32_16x16x128_f8f6f4 v[50:53], v[26:33], v[196:203], v[50:53], v187, v187 op_sel_hi:[0,0,0]
	v_mfma_scale_f32_16x16x128_f8f6f4 v[46:49], v[18:25], v[204:211], v[46:49], v187, v187 op_sel_hi:[0,0,0]
	v_mfma_scale_f32_16x16x128_f8f6f4 v[42:45], v[26:33], v[204:211], v[42:45], v187, v187 op_sel_hi:[0,0,0]
	v_mfma_scale_f32_16x16x128_f8f6f4 v[38:41], v[18:25], v[212:219], v[38:41], v187, v187 op_sel_hi:[0,0,0]
	v_mfma_scale_f32_16x16x128_f8f6f4 v[34:37], v[26:33], v[212:219], v[34:37], v187, v187 op_sel_hi:[0,0,0]
	s_cbranch_vccz .Lwb_1577l_3
	s_waitcnt vmcnt(8)
.Lwb_1577l_3:
	s_setprio 0
	s_barrier
	s_add_i32 s71, s71, 2
	s_add_u32 s69, s69, 0x4000
	s_addc_u32 s70, s70, 0
	s_add_u32 s40, s40, 0x100
	s_addc_u32 s41, s41, 0
	s_cmp_gt_u32 s71, 13
	s_cbranch_scc0 .LBB0_1577
	s_and_b64 vcc, exec, s[16:17]
	s_cbranch_vccz .LBB0_1580
	s_barrier
